# adds: K-loop load segments use one combined vmcnt/lgkmcnt wait and drop the m0 hazard nop where the address VALU op can sit between the m0 write and the LDS-DMA
# speedup vs baseline: 1.0105x; 1.0040x over previous
; #define PG8_GREAD(dst, u, par) do { _Pragma("unroll") for (int h_ = 0; h_ < 2; ++h_) _Pragma("unroll") for (int i_ = 0; i_ < 2; ++i_) { const int rl_ = 128 * h_ + grl[i_]; \
;         const int tk_ = *(const PG8_LAS int*)(gtab + (par) * 2048 + rl_ * 8); const unsigned tok_ = (rl_ < (u).rows) ? ((unsigned)tk_ >> 2) : 0u; dst[h_][i_] = tok_ * (unsigned)(K * 2) + gcb[i_]; } } while (0)
; #define PG8_STAGE(bufoff, gbase, voff) do { _Pragma("unroll") for (int _i = 0; _i < 2; ++_i) \
;         __builtin_amdgcn_global_load_lds((const unsigned*)((const char*)(gbase) + (voff)[_i]), (PG8_LAS unsigned*)(lds + (bufoff) + ldsw + _i * 8192), 16, 0, 0); } while (0)
; #define PG8_LDA(dst, b, h) do { _Pragma("unroll") for (int m = 0; m < 4; ++m) _Pragma("unroll") for (int k = 0; k < 2; ++k) dst[m][k] = *(const PG8_LAS bf16x8*)(lds + PG8_SA(b, h) + aoff + m * 2048 + k * 1024); } while (0)
; template <class Epi, class Sched, bool ALIGN_EPI = false, bool SP2 = false, bool GATHER = false>
; __device__ __forceinline__ void gemm_phase(PG8_LAS unsigned char* lds, const Gemm g, const Sched& S, const Epi& E, const int2* gslot = nullptr, PG8_LAS unsigned char* gtab = nullptr) {
;     ...
;             const char* a1 = cA + (size_t)(t + 1) * kstep;
;             const char* a2 = last ? nA : cA + (size_t)(t + 2) * kstep; const char* b2 = last ? nB : cB + (size_t)(t + 2) * kstep;
;             const char* a3 = a2 + kstep; const char* b3 = b2 + kstep;
;             if (last && has_next) S.a_ready(nxt);
;             if constexpr (GATHER) { if (last) { if (has_next) { PG8_GREAD(vN, nxt, (ui + 1) & 1); } else { _Pragma("unroll") for (int h_ = 0; h_ < 2; ++h_) _Pragma("unroll") for (int i_ = 0; i_ < 2; ++i_) vN[h_][i_] = vC[h_][i_]; } } }
;             unsigned vS[2][2];
; #pragma unroll
;             for (int h_ = 0; h_ < 2; ++h_)
; #pragma unroll
;                 for (int i_ = 0; i_ < 2; ++i_) vS[h_][i_] = (GATHER && last) ? vN[h_][i_] : vC[h_][i_];
;             if constexpr (SP2) {
;             PG8_LDB(B0, 0, 0); PG8_LDB(B1, 0, 1); PG8_SCHED; PG8_LDA(At, 0, 0); PG8_STAGE(PG8_SA(1, 1), a1 + PG8_AH(1), PG8_VA(vC, 1));
;             PG8_WAIT_V(8); PG8_WAIT_L(0); PG8_BAR; PG8_MMA(0, 0, At, B0); PG8_MMA(0, 1, At, B1); PG8_BAR; PG8_SCHED;
;             PG8_LDA(At, 0, 1); PG8_STAGE(PG8_SB(0, 0), b2, voffB); PG8_STAGE(PG8_SB(0, 1), b2 + hstep, voffB); PG8_STAGE(PG8_SA(0, 0), a2, PG8_VA(vS, 0));
.LBB0_131:
	s_add_u32 s2, s8, 0xfffc0080
	s_addc_u32 s10, s9, -1
	s_cmp_eq_u32 s34, 12
	s_cselect_b32 s27, s21, s10
	s_cselect_b32 s26, s28, s2
	s_cselect_b32 s11, s19, s31
	s_cselect_b32 s10, s29, s30
	s_add_i32 s2, 0, 0x10000
	v_add_u32_e32 v0, s2, v143
	s_add_i32 s35, 0, 0x14000
	ds_read_b128 v[146:149], v0
	ds_read_b128 v[150:153], v0 offset:1024
	ds_read_b128 v[154:157], v0 offset:2048
	ds_read_b128 v[158:161], v0 offset:3072
	v_add_u32_e32 v0, s35, v143
	ds_read_b128 v[162:165], v0
	ds_read_b128 v[166:169], v0 offset:1024
	ds_read_b128 v[170:173], v0 offset:2048
	ds_read_b128 v[174:177], v0 offset:3072
	v_lshl_add_u64 v[210:211], s[8:9], 0, v[138:139]
	s_add_i32 m0, s46, 0xc000
	ds_read_b128 v[178:181], v145
	ds_read_b128 v[182:185], v145 offset:1024
	ds_read_b128 v[186:189], v145 offset:2048
	ds_read_b128 v[190:193], v145 offset:3072
	ds_read_b128 v[194:197], v145 offset:4096
	ds_read_b128 v[198:201], v145 offset:5120
	ds_read_b128 v[202:205], v145 offset:6144
	ds_read_b128 v[206:209], v145 offset:7168
	global_load_lds_dwordx4 v[210:211], off
	s_add_i32 m0, s46, 0xe000
	v_lshl_add_u64 v[210:211], s[8:9], 0, v[140:141]
	global_load_lds_dwordx4 v[210:211], off
	s_waitcnt vmcnt(8) lgkmcnt(0)
	s_setprio 1
	s_barrier
	v_mfma_f32_16x16x32_bf16 v[126:129], v[146:149], v[178:181], v[126:129]
	v_mfma_f32_16x16x32_bf16 v[122:125], v[154:157], v[178:181], v[122:125]
	v_mfma_f32_16x16x32_bf16 v[118:121], v[146:149], v[186:189], v[118:121]
	v_mfma_f32_16x16x32_bf16 v[114:117], v[154:157], v[186:189], v[114:117]
	v_mfma_f32_16x16x32_bf16 v[110:113], v[146:149], v[194:197], v[110:113]
	v_mfma_f32_16x16x32_bf16 v[106:109], v[154:157], v[194:197], v[106:109]
	v_mfma_f32_16x16x32_bf16 v[102:105], v[146:149], v[202:205], v[102:105]
	v_mfma_f32_16x16x32_bf16 v[98:101], v[154:157], v[202:205], v[98:101]
	v_mfma_f32_16x16x32_bf16 v[126:129], v[150:153], v[182:185], v[126:129]
	v_mfma_f32_16x16x32_bf16 v[122:125], v[158:161], v[182:185], v[122:125]
	v_mfma_f32_16x16x32_bf16 v[118:121], v[150:153], v[190:193], v[118:121]
	v_mfma_f32_16x16x32_bf16 v[114:117], v[158:161], v[190:193], v[114:117]
	v_mfma_f32_16x16x32_bf16 v[110:113], v[150:153], v[198:201], v[110:113]
	v_mfma_f32_16x16x32_bf16 v[106:109], v[158:161], v[198:201], v[106:109]
	v_mfma_f32_16x16x32_bf16 v[102:105], v[150:153], v[206:209], v[102:105]
	v_mfma_f32_16x16x32_bf16 v[98:101], v[158:161], v[206:209], v[98:101]
	v_mfma_f32_16x16x32_bf16 v[62:65], v[162:165], v[178:181], v[62:65]
	v_mfma_f32_16x16x32_bf16 v[58:61], v[170:173], v[178:181], v[58:61]
	v_mfma_f32_16x16x32_bf16 v[54:57], v[162:165], v[186:189], v[54:57]
	v_mfma_f32_16x16x32_bf16 v[50:53], v[170:173], v[186:189], v[50:53]
	v_mfma_f32_16x16x32_bf16 v[46:49], v[162:165], v[194:197], v[46:49]
	v_mfma_f32_16x16x32_bf16 v[42:45], v[170:173], v[194:197], v[42:45]
	v_mfma_f32_16x16x32_bf16 v[38:41], v[162:165], v[202:205], v[38:41]
	v_mfma_f32_16x16x32_bf16 v[34:37], v[170:173], v[202:205], v[34:37]
	v_mfma_f32_16x16x32_bf16 v[62:65], v[166:169], v[182:185], v[62:65]
	v_mfma_f32_16x16x32_bf16 v[58:61], v[174:177], v[182:185], v[58:61]
	v_mfma_f32_16x16x32_bf16 v[54:57], v[166:169], v[190:193], v[54:57]
	v_mfma_f32_16x16x32_bf16 v[50:53], v[174:177], v[190:193], v[50:53]
	v_mfma_f32_16x16x32_bf16 v[46:49], v[166:169], v[198:201], v[46:49]
	v_mfma_f32_16x16x32_bf16 v[42:45], v[174:177], v[198:201], v[42:45]
	v_mfma_f32_16x16x32_bf16 v[38:41], v[166:169], v[206:209], v[38:41]
	v_mfma_f32_16x16x32_bf16 v[34:37], v[174:177], v[206:209], v[34:37]
	s_barrier
	s_setprio 0
	s_add_i32 s2, s2, s45
	v_lshl_add_u64 v[210:211], s[10:11], 0, v[134:135]
	s_mov_b32 m0, s2
	ds_read_b128 v[178:181], v145 offset:16384
	ds_read_b128 v[182:185], v145 offset:17408
	ds_read_b128 v[186:189], v145 offset:18432
	ds_read_b128 v[190:193], v145 offset:19456
	ds_read_b128 v[194:197], v145 offset:20480
	ds_read_b128 v[198:201], v145 offset:21504
	ds_read_b128 v[202:205], v145 offset:22528
	ds_read_b128 v[206:209], v145 offset:23552
	global_load_lds_dwordx4 v[210:211], off
	s_add_i32 m0, s2, 0x2000
	s_add_u32 s36, s10, 0x40000
	v_lshl_add_u64 v[212:213], s[10:11], 0, v[130:131]
	s_addc_u32 s37, s11, 0
	s_add_i32 s2, s35, s45
	global_load_lds_dwordx4 v[212:213], off
	v_lshl_add_u64 v[214:215], s[36:37], 0, v[134:135]
	s_mov_b32 m0, s2
	v_lshl_add_u64 v[216:217], s[26:27], 0, v[132:133]
	global_load_lds_dwordx4 v[214:215], off
	s_add_i32 m0, s2, 0x2000
	v_lshl_add_u64 v[214:215], s[36:37], 0, v[130:131]
	global_load_lds_dwordx4 v[214:215], off
	s_mov_b32 m0, s46
	v_lshl_add_u64 v[214:215], s[26:27], 0, v[136:137]
	global_load_lds_dwordx4 v[214:215], off
	s_mov_b32 m0, s47
	s_nop 0
	global_load_lds_dwordx4 v[216:217], off
	s_waitcnt vmcnt(8) lgkmcnt(0)
	s_setprio 1
	s_barrier
; #define PG8_STAGE(bufoff, gbase, voff) do { _Pragma("unroll") for (int _i = 0; _i < 2; ++_i) \
;         __builtin_amdgcn_global_load_lds((const unsigned*)((const char*)(gbase) + (voff)[_i]), (PG8_LAS unsigned*)(lds + (bufoff) + ldsw + _i * 8192), 16, 0, 0); } while (0)
; #define PG8_LDA(dst, b, h) do { _Pragma("unroll") for (int m = 0; m < 4; ++m) _Pragma("unroll") for (int k = 0; k < 2; ++k) dst[m][k] = *(const PG8_LAS bf16x8*)(lds + PG8_SA(b, h) + aoff + m * 2048 + k * 1024); } while (0)
; #define PG8_LDB(dst, b, h) do { _Pragma("unroll") for (int n = 0; n < 2; ++n) _Pragma("unroll") for (int k = 0; k < 2; ++k) dst[n][k] = *(const PG8_LAS bf16x8*)(lds + PG8_SB(b, h) + boff + n * 2048 + k * 1024); } while (0)
; #define PG8_MMA(ai, bj, At, Bt) do { __builtin_amdgcn_s_setprio(1); _Pragma("unroll") for (int m = 0; m < 4; ++m) _Pragma("unroll") for (int n = 0; n < 2; ++n) _Pragma("unroll") for (int k = 0; k < 2; ++k) \
;         acc[ai][bj][m][n] = __builtin_amdgcn_mfma_f32_16x16x32_bf16(Bt[n][k], At[m][k], acc[ai][bj][m][n], 0, 0, 0); __builtin_amdgcn_s_setprio(0); } while (0)
; #define PG8_WAIT_V(n) asm volatile("s_waitcnt vmcnt(" #n ")" ::: "memory")
; #define PG8_WAIT_L(n) asm volatile("s_waitcnt lgkmcnt(" #n ")" ::: "memory")
; #define PG8_BAR __builtin_amdgcn_s_barrier()
; #define PG8_SCHED __builtin_amdgcn_sched_barrier(0)
; template <class Epi, class Sched, bool ALIGN_EPI = false, bool SP2 = false, bool GATHER = false>
; __device__ __forceinline__ void gemm_phase(PG8_LAS unsigned char* lds, const Gemm g, const Sched& S, const Epi& E, const int2* gslot = nullptr, PG8_LAS unsigned char* gtab = nullptr) {
;     ...
;             PG8_WAIT_V(8); PG8_WAIT_L(0); PG8_BAR; PG8_MMA(1, 0, At, B0); PG8_MMA(1, 1, At, B1); PG8_BAR; PG8_SCHED;
;             PG8_LDB(B0, 1, 0); PG8_LDB(B1, 1, 1); PG8_SCHED; PG8_LDA(At, 1, 0); PG8_STAGE(PG8_SA(0, 1), a2 + PG8_AH(1), PG8_VA(vS, 1));
;             PG8_WAIT_V(8); PG8_WAIT_L(0); PG8_BAR; PG8_MMA(0, 0, At, B0); PG8_MMA(0, 1, At, B1); PG8_BAR; PG8_SCHED;
	v_mfma_f32_16x16x32_bf16 v[94:97], v[146:149], v[178:181], v[94:97]
	v_mfma_f32_16x16x32_bf16 v[90:93], v[154:157], v[178:181], v[90:93]
	v_mfma_f32_16x16x32_bf16 v[86:89], v[146:149], v[186:189], v[86:89]
	v_mfma_f32_16x16x32_bf16 v[82:85], v[154:157], v[186:189], v[82:85]
	v_mfma_f32_16x16x32_bf16 v[78:81], v[146:149], v[194:197], v[78:81]
	v_mfma_f32_16x16x32_bf16 v[74:77], v[154:157], v[194:197], v[74:77]
	v_mfma_f32_16x16x32_bf16 v[70:73], v[146:149], v[202:205], v[70:73]
	v_mfma_f32_16x16x32_bf16 v[66:69], v[154:157], v[202:205], v[66:69]
	v_mfma_f32_16x16x32_bf16 v[94:97], v[150:153], v[182:185], v[94:97]
	v_mfma_f32_16x16x32_bf16 v[90:93], v[158:161], v[182:185], v[90:93]
	v_mfma_f32_16x16x32_bf16 v[86:89], v[150:153], v[190:193], v[86:89]
	v_mfma_f32_16x16x32_bf16 v[82:85], v[158:161], v[190:193], v[82:85]
	v_mfma_f32_16x16x32_bf16 v[78:81], v[150:153], v[198:201], v[78:81]
	v_mfma_f32_16x16x32_bf16 v[74:77], v[158:161], v[198:201], v[74:77]
	v_mfma_f32_16x16x32_bf16 v[70:73], v[150:153], v[206:209], v[70:73]
	v_mfma_f32_16x16x32_bf16 v[66:69], v[158:161], v[206:209], v[66:69]
	v_mfma_f32_16x16x32_bf16 v[30:33], v[162:165], v[178:181], v[30:33]
	v_mfma_f32_16x16x32_bf16 v[26:29], v[170:173], v[178:181], v[26:29]
	v_mfma_f32_16x16x32_bf16 v[22:25], v[162:165], v[186:189], v[22:25]
	v_mfma_f32_16x16x32_bf16 v[18:21], v[170:173], v[186:189], v[18:21]
	v_mfma_f32_16x16x32_bf16 v[14:17], v[162:165], v[194:197], v[14:17]
	v_mfma_f32_16x16x32_bf16 v[10:13], v[170:173], v[194:197], v[10:13]
	v_mfma_f32_16x16x32_bf16 v[6:9], v[162:165], v[202:205], v[6:9]
	v_mfma_f32_16x16x32_bf16 v[2:5], v[170:173], v[202:205], v[2:5]
	v_mfma_f32_16x16x32_bf16 v[30:33], v[166:169], v[182:185], v[30:33]
	v_mfma_f32_16x16x32_bf16 v[26:29], v[174:177], v[182:185], v[26:29]
	v_mfma_f32_16x16x32_bf16 v[22:25], v[166:169], v[190:193], v[22:25]
	v_mfma_f32_16x16x32_bf16 v[18:21], v[174:177], v[190:193], v[18:21]
	v_mfma_f32_16x16x32_bf16 v[14:17], v[166:169], v[198:201], v[14:17]
	v_mfma_f32_16x16x32_bf16 v[10:13], v[174:177], v[198:201], v[10:13]
	v_mfma_f32_16x16x32_bf16 v[6:9], v[166:169], v[206:209], v[6:9]
	v_mfma_f32_16x16x32_bf16 v[2:5], v[174:177], v[206:209], v[2:5]
	s_barrier
	s_setprio 0
	s_add_i32 s2, 0, 0x18000
	v_add_u32_e32 v0, s2, v143
	s_add_i32 s35, 0, 0x1c000
	ds_read_b128 v[146:149], v0
	ds_read_b128 v[150:153], v0 offset:1024
	ds_read_b128 v[154:157], v0 offset:2048
	ds_read_b128 v[158:161], v0 offset:3072
	v_add_u32_e32 v0, s35, v143
	ds_read_b128 v[162:165], v0
	ds_read_b128 v[166:169], v0 offset:1024
	ds_read_b128 v[170:173], v0 offset:2048
	ds_read_b128 v[174:177], v0 offset:3072
	s_add_u32 s26, s26, 0x40000
	s_addc_u32 s27, s27, 0
	s_mov_b32 m0, s50
	v_lshl_add_u64 v[218:219], s[26:27], 0, v[136:137]
	ds_read_b128 v[178:181], v145 offset:32768
	ds_read_b128 v[182:185], v145 offset:33792
	ds_read_b128 v[186:189], v145 offset:34816
	ds_read_b128 v[190:193], v145 offset:35840
	ds_read_b128 v[194:197], v145 offset:36864
	ds_read_b128 v[198:201], v145 offset:37888
	ds_read_b128 v[202:205], v145 offset:38912
	ds_read_b128 v[206:209], v145 offset:39936
	global_load_lds_dwordx4 v[218:219], off
	s_mov_b32 m0, s51
	v_lshl_add_u64 v[218:219], s[26:27], 0, v[132:133]
	global_load_lds_dwordx4 v[218:219], off
	s_waitcnt vmcnt(8) lgkmcnt(0)
	s_setprio 1
	s_barrier
	v_mfma_f32_16x16x32_bf16 v[126:129], v[146:149], v[178:181], v[126:129]
	v_mfma_f32_16x16x32_bf16 v[122:125], v[154:157], v[178:181], v[122:125]
	v_mfma_f32_16x16x32_bf16 v[118:121], v[146:149], v[186:189], v[118:121]
	v_mfma_f32_16x16x32_bf16 v[114:117], v[154:157], v[186:189], v[114:117]
	v_mfma_f32_16x16x32_bf16 v[110:113], v[146:149], v[194:197], v[110:113]
	v_mfma_f32_16x16x32_bf16 v[106:109], v[154:157], v[194:197], v[106:109]
	v_mfma_f32_16x16x32_bf16 v[102:105], v[146:149], v[202:205], v[102:105]
	v_mfma_f32_16x16x32_bf16 v[98:101], v[154:157], v[202:205], v[98:101]
	v_mfma_f32_16x16x32_bf16 v[126:129], v[150:153], v[182:185], v[126:129]
	v_mfma_f32_16x16x32_bf16 v[122:125], v[158:161], v[182:185], v[122:125]
	v_mfma_f32_16x16x32_bf16 v[118:121], v[150:153], v[190:193], v[118:121]
	v_mfma_f32_16x16x32_bf16 v[114:117], v[158:161], v[190:193], v[114:117]
	v_mfma_f32_16x16x32_bf16 v[110:113], v[150:153], v[198:201], v[110:113]
	v_mfma_f32_16x16x32_bf16 v[106:109], v[158:161], v[198:201], v[106:109]
	v_mfma_f32_16x16x32_bf16 v[102:105], v[150:153], v[206:209], v[102:105]
	v_mfma_f32_16x16x32_bf16 v[98:101], v[158:161], v[206:209], v[98:101]
	v_mfma_f32_16x16x32_bf16 v[62:65], v[162:165], v[178:181], v[62:65]
	v_mfma_f32_16x16x32_bf16 v[58:61], v[170:173], v[178:181], v[58:61]
	v_mfma_f32_16x16x32_bf16 v[54:57], v[162:165], v[186:189], v[54:57]
	v_mfma_f32_16x16x32_bf16 v[50:53], v[170:173], v[186:189], v[50:53]
	v_mfma_f32_16x16x32_bf16 v[46:49], v[162:165], v[194:197], v[46:49]
	v_mfma_f32_16x16x32_bf16 v[42:45], v[170:173], v[194:197], v[42:45]
	v_mfma_f32_16x16x32_bf16 v[38:41], v[162:165], v[202:205], v[38:41]
	v_mfma_f32_16x16x32_bf16 v[34:37], v[170:173], v[202:205], v[34:37]
	v_mfma_f32_16x16x32_bf16 v[62:65], v[166:169], v[182:185], v[62:65]
	v_mfma_f32_16x16x32_bf16 v[58:61], v[174:177], v[182:185], v[58:61]
	v_mfma_f32_16x16x32_bf16 v[54:57], v[166:169], v[190:193], v[54:57]
	v_mfma_f32_16x16x32_bf16 v[50:53], v[174:177], v[190:193], v[50:53]
	v_mfma_f32_16x16x32_bf16 v[46:49], v[166:169], v[198:201], v[46:49]
	v_mfma_f32_16x16x32_bf16 v[42:45], v[174:177], v[198:201], v[42:45]
	v_mfma_f32_16x16x32_bf16 v[38:41], v[166:169], v[206:209], v[38:41]
	v_mfma_f32_16x16x32_bf16 v[34:37], v[174:177], v[206:209], v[34:37]
	s_barrier
; #define PG8_STAGE(bufoff, gbase, voff) do { _Pragma("unroll") for (int _i = 0; _i < 2; ++_i) \
;         __builtin_amdgcn_global_load_lds((const unsigned*)((const char*)(gbase) + (voff)[_i]), (PG8_LAS unsigned*)(lds + (bufoff) + ldsw + _i * 8192), 16, 0, 0); } while (0)
; #define PG8_LDA(dst, b, h) do { _Pragma("unroll") for (int m = 0; m < 4; ++m) _Pragma("unroll") for (int k = 0; k < 2; ++k) dst[m][k] = *(const PG8_LAS bf16x8*)(lds + PG8_SA(b, h) + aoff + m * 2048 + k * 1024); } while (0)
; #define PG8_MMA(ai, bj, At, Bt) do { __builtin_amdgcn_s_setprio(1); _Pragma("unroll") for (int m = 0; m < 4; ++m) _Pragma("unroll") for (int n = 0; n < 2; ++n) _Pragma("unroll") for (int k = 0; k < 2; ++k) \
;         acc[ai][bj][m][n] = __builtin_amdgcn_mfma_f32_16x16x32_bf16(Bt[n][k], At[m][k], acc[ai][bj][m][n], 0, 0, 0); __builtin_amdgcn_s_setprio(0); } while (0)
; #define PG8_WAIT_V(n) asm volatile("s_waitcnt vmcnt(" #n ")" ::: "memory")
; #define PG8_WAIT_L(n) asm volatile("s_waitcnt lgkmcnt(" #n ")" ::: "memory")
; #define PG8_BAR __builtin_amdgcn_s_barrier()
; #define PG8_SCHED __builtin_amdgcn_sched_barrier(0)
; template <class Epi, class Sched, bool ALIGN_EPI = false, bool SP2 = false, bool GATHER = false>
; __device__ __forceinline__ void gemm_phase(PG8_LAS unsigned char* lds, const Gemm g, const Sched& S, const Epi& E, const int2* gslot = nullptr, PG8_LAS unsigned char* gtab = nullptr) {
;     ...
;         for (int t = 0; t < nt; t += 2) {
;             const bool last = (t == nt - 2);
;             const char* a1 = cA + (size_t)(t + 1) * kstep;
;             const char* a2 = last ? nA : cA + (size_t)(t + 2) * kstep; const char* b2 = last ? nB : cB + (size_t)(t + 2) * kstep;
;             const char* a3 = a2 + kstep; const char* b3 = b2 + kstep;
;             if (last && has_next) S.a_ready(nxt);
;     ...
;             PG8_LDA(At, 1, 1); PG8_STAGE(PG8_SB(1, 0), b3, voffB); PG8_STAGE(PG8_SB(1, 1), b3 + hstep, voffB); PG8_STAGE(PG8_SA(1, 0), a3, PG8_VA(vS, 0));
;             PG8_WAIT_V(8); PG8_WAIT_L(0); PG8_BAR; PG8_MMA(1, 0, At, B0); PG8_MMA(1, 1, At, B1); PG8_BAR; PG8_SCHED;
	s_setprio 0
	s_add_i32 s2, s2, s45
	v_lshl_add_u64 v[210:211], v[210:211], 0, s[54:55]
	s_mov_b32 m0, s2
	ds_read_b128 v[178:181], v145 offset:49152
	ds_read_b128 v[182:185], v145 offset:50176
	ds_read_b128 v[186:189], v145 offset:51200
	ds_read_b128 v[190:193], v145 offset:52224
	ds_read_b128 v[194:197], v145 offset:53248
	ds_read_b128 v[198:201], v145 offset:54272
	ds_read_b128 v[202:205], v145 offset:55296
	ds_read_b128 v[206:209], v145 offset:56320
	global_load_lds_dwordx4 v[210:211], off
	s_add_i32 m0, s2, 0x2000
	s_add_u32 s10, s10, 0x40080
	v_lshl_add_u64 v[210:211], v[212:213], 0, s[54:55]
	s_addc_u32 s11, s11, 0
	s_add_i32 s2, s35, s45
	global_load_lds_dwordx4 v[210:211], off
	s_mov_b32 m0, s2
	v_lshl_add_u64 v[210:211], s[10:11], 0, v[134:135]
	global_load_lds_dwordx4 v[210:211], off
	s_add_i32 m0, s2, 0x2000
	v_lshl_add_u64 v[210:211], s[10:11], 0, v[130:131]
	global_load_lds_dwordx4 v[210:211], off
	s_mov_b32 m0, s60
	v_lshl_add_u64 v[210:211], v[214:215], 0, s[54:55]
	global_load_lds_dwordx4 v[210:211], off
	s_mov_b32 m0, s61
	v_lshl_add_u64 v[210:211], v[216:217], 0, s[54:55]
	global_load_lds_dwordx4 v[210:211], off
	s_waitcnt vmcnt(8) lgkmcnt(0)
	s_setprio 1
	s_barrier
	v_mfma_f32_16x16x32_bf16 v[94:97], v[146:149], v[178:181], v[94:97]
	v_mfma_f32_16x16x32_bf16 v[90:93], v[154:157], v[178:181], v[90:93]
	v_mfma_f32_16x16x32_bf16 v[86:89], v[146:149], v[186:189], v[86:89]
	v_mfma_f32_16x16x32_bf16 v[82:85], v[154:157], v[186:189], v[82:85]
	v_mfma_f32_16x16x32_bf16 v[78:81], v[146:149], v[194:197], v[78:81]
	v_mfma_f32_16x16x32_bf16 v[74:77], v[154:157], v[194:197], v[74:77]
	v_mfma_f32_16x16x32_bf16 v[70:73], v[146:149], v[202:205], v[70:73]
	v_mfma_f32_16x16x32_bf16 v[66:69], v[154:157], v[202:205], v[66:69]
	v_mfma_f32_16x16x32_bf16 v[94:97], v[150:153], v[182:185], v[94:97]
	v_mfma_f32_16x16x32_bf16 v[90:93], v[158:161], v[182:185], v[90:93]
	v_mfma_f32_16x16x32_bf16 v[86:89], v[150:153], v[190:193], v[86:89]
	v_mfma_f32_16x16x32_bf16 v[82:85], v[158:161], v[190:193], v[82:85]
	v_mfma_f32_16x16x32_bf16 v[78:81], v[150:153], v[198:201], v[78:81]
	v_mfma_f32_16x16x32_bf16 v[74:77], v[158:161], v[198:201], v[74:77]
	v_mfma_f32_16x16x32_bf16 v[70:73], v[150:153], v[206:209], v[70:73]
	v_mfma_f32_16x16x32_bf16 v[66:69], v[158:161], v[206:209], v[66:69]
	v_mfma_f32_16x16x32_bf16 v[30:33], v[162:165], v[178:181], v[30:33]
	v_mfma_f32_16x16x32_bf16 v[26:29], v[170:173], v[178:181], v[26:29]
	v_mfma_f32_16x16x32_bf16 v[22:25], v[162:165], v[186:189], v[22:25]
	v_mfma_f32_16x16x32_bf16 v[18:21], v[170:173], v[186:189], v[18:21]
	v_mfma_f32_16x16x32_bf16 v[14:17], v[162:165], v[194:197], v[14:17]
	v_mfma_f32_16x16x32_bf16 v[10:13], v[170:173], v[194:197], v[10:13]
	v_mfma_f32_16x16x32_bf16 v[6:9], v[162:165], v[202:205], v[6:9]
	v_mfma_f32_16x16x32_bf16 v[2:5], v[170:173], v[202:205], v[2:5]
	v_mfma_f32_16x16x32_bf16 v[30:33], v[166:169], v[182:185], v[30:33]
	v_mfma_f32_16x16x32_bf16 v[26:29], v[174:177], v[182:185], v[26:29]
	v_mfma_f32_16x16x32_bf16 v[22:25], v[166:169], v[190:193], v[22:25]
	v_mfma_f32_16x16x32_bf16 v[18:21], v[174:177], v[190:193], v[18:21]
	v_mfma_f32_16x16x32_bf16 v[14:17], v[166:169], v[198:201], v[14:17]
	v_mfma_f32_16x16x32_bf16 v[10:13], v[174:177], v[198:201], v[10:13]
	v_mfma_f32_16x16x32_bf16 v[6:9], v[166:169], v[206:209], v[6:9]
	v_mfma_f32_16x16x32_bf16 v[2:5], v[174:177], v[206:209], v[2:5]
	s_barrier
	s_setprio 0
	s_add_i32 s34, s34, 2
	s_add_u32 s8, s8, 0x100
	s_addc_u32 s9, s9, 0
	s_add_u32 s30, s30, 0x100
	s_addc_u32 s31, s31, 0
	s_cmp_gt_u32 s34, 13
	s_cbranch_scc0 .LBB0_131
	s_and_b64 vcc, exec, s[14:15]
	s_cbranch_vccz .LBB0_134
	s_barrier

; #define PG8_GREAD(dst, u, par) do { _Pragma("unroll") for (int h_ = 0; h_ < 2; ++h_) _Pragma("unroll") for (int i_ = 0; i_ < 2; ++i_) { const int rl_ = 128 * h_ + grl[i_]; \
;         const int tk_ = *(const PG8_LAS int*)(gtab + (par) * 2048 + rl_ * 8); const unsigned tok_ = (rl_ < (u).rows) ? ((unsigned)tk_ >> 2) : 0u; dst[h_][i_] = tok_ * (unsigned)(K * 2) + gcb[i_]; } } while (0)
; #define PG8_STAGE(bufoff, gbase, voff) do { _Pragma("unroll") for (int _i = 0; _i < 2; ++_i) \
;         __builtin_amdgcn_global_load_lds((const unsigned*)((const char*)(gbase) + (voff)[_i]), (PG8_LAS unsigned*)(lds + (bufoff) + ldsw + _i * 8192), 16, 0, 0); } while (0)
; #define PG8_WAIT_V(n) asm volatile("s_waitcnt vmcnt(" #n ")" ::: "memory")
; #define PG8_WAIT_L(n) asm volatile("s_waitcnt lgkmcnt(" #n ")" ::: "memory")
; template <class Epi, class Sched, bool ALIGN_EPI = false, bool SP2 = false, bool GATHER = false>
; __device__ __forceinline__ void gemm_phase(PG8_LAS unsigned char* lds, const Gemm g, const Sched& S, const Epi& E, const int2* gslot = nullptr, PG8_LAS unsigned char* gtab = nullptr) {
;     ...
;             const bool last = (t == nt - 2);
;             const char* a1 = cA + (size_t)(t + 1) * kstep;
;             const char* a2 = last ? nA : cA + (size_t)(t + 2) * kstep; const char* b2 = last ? nB : cB + (size_t)(t + 2) * kstep;
;             const char* a3 = a2 + kstep; const char* b3 = b2 + kstep;
;             if (last && has_next) S.a_ready(nxt);
;             if constexpr (GATHER) { if (last) { if (has_next) { PG8_GREAD(vN, nxt, (ui + 1) & 1); } else { _Pragma("unroll") for (int h_ = 0; h_ < 2; ++h_) _Pragma("unroll") for (int i_ = 0; i_ < 2; ++i_) vN[h_][i_] = vC[h_][i_]; } } }
;             unsigned vS[2][2];
; #pragma unroll
;             for (int h_ = 0; h_ < 2; ++h_)
; #pragma unroll
;                 for (int i_ = 0; i_ < 2; ++i_) vS[h_][i_] = (GATHER && last) ? vN[h_][i_] : vC[h_][i_];
;             if constexpr (SP2) {
;             PG8_LDB(B0, 0, 0); PG8_LDB(B1, 0, 1); PG8_SCHED; PG8_LDA(At, 0, 0); PG8_STAGE(PG8_SA(1, 1), a1 + PG8_AH(1), PG8_VA(vC, 1));
;             PG8_WAIT_V(8); PG8_WAIT_L(0); PG8_BAR; PG8_MMA(0, 0, At, B0); PG8_MMA(0, 1, At, B1); PG8_BAR; PG8_SCHED;
;             PG8_LDA(At, 0, 1); PG8_STAGE(PG8_SB(0, 0), b2, voffB); PG8_STAGE(PG8_SB(0, 1), b2 + hstep, voffB); PG8_STAGE(PG8_SA(0, 0), a2, PG8_VA(vS, 0));
.LBB0_482:
	s_add_u32 s34, s30, 0x100
	s_addc_u32 s35, s31, 0
	s_cmp_eq_u32 s66, 28
	s_cselect_b32 s39, s25, s35
	s_cselect_b32 s38, s62, s34
	s_cselect_b32 s37, s23, s65
	s_cselect_b32 s36, s63, s64
	s_add_i32 s2, 0, 0x10000
	s_add_i32 s67, 0, 0x14000
	v_add_u32_e32 v148, s2, v215
	v_add_u32_e32 v164, s67, v215
	ds_read_b128 v[136:139], v148
	ds_read_b128 v[140:143], v148 offset:1024
	ds_read_b128 v[144:147], v148 offset:2048
	ds_read_b128 v[148:151], v148 offset:3072
	ds_read_b128 v[152:155], v164
	ds_read_b128 v[156:159], v164 offset:1024
	ds_read_b128 v[160:163], v164 offset:2048
	ds_read_b128 v[164:167], v164 offset:3072
	v_lshl_add_u64 v[202:203], s[30:31], 0, v[132:133]
	s_add_i32 m0, s46, 0xc000
	ds_read_b128 v[168:171], v181
	ds_read_b128 v[172:175], v181 offset:1024
	ds_read_b128 v[176:179], v181 offset:2048
	ds_read_b128 v[182:185], v181 offset:3072
	ds_read_b128 v[186:189], v181 offset:4096
	ds_read_b128 v[190:193], v181 offset:5120
	ds_read_b128 v[194:197], v181 offset:6144
	ds_read_b128 v[198:201], v181 offset:7168
	global_load_lds_dwordx4 v[202:203], off
	s_add_i32 m0, s46, 0xe000
	v_lshl_add_u64 v[202:203], s[30:31], 0, v[134:135]
	global_load_lds_dwordx4 v[202:203], off
	s_waitcnt vmcnt(8) lgkmcnt(0)
	s_setprio 1
	s_barrier
	v_mfma_f32_16x16x32_bf16 v[126:129], v[136:139], v[168:171], v[126:129]
	v_mfma_f32_16x16x32_bf16 v[122:125], v[144:147], v[168:171], v[122:125]
	v_mfma_f32_16x16x32_bf16 v[110:113], v[136:139], v[176:179], v[110:113]
	v_mfma_f32_16x16x32_bf16 v[106:109], v[144:147], v[176:179], v[106:109]
	v_mfma_f32_16x16x32_bf16 v[94:97], v[136:139], v[186:189], v[94:97]
	v_mfma_f32_16x16x32_bf16 v[90:93], v[144:147], v[186:189], v[90:93]
	v_mfma_f32_16x16x32_bf16 v[78:81], v[136:139], v[194:197], v[78:81]
	v_mfma_f32_16x16x32_bf16 v[74:77], v[144:147], v[194:197], v[74:77]
	v_mfma_f32_16x16x32_bf16 v[126:129], v[140:143], v[172:175], v[126:129]
	v_mfma_f32_16x16x32_bf16 v[122:125], v[148:151], v[172:175], v[122:125]
	v_mfma_f32_16x16x32_bf16 v[110:113], v[140:143], v[182:185], v[110:113]
	v_mfma_f32_16x16x32_bf16 v[106:109], v[148:151], v[182:185], v[106:109]
	v_mfma_f32_16x16x32_bf16 v[94:97], v[140:143], v[190:193], v[94:97]
	v_mfma_f32_16x16x32_bf16 v[90:93], v[148:151], v[190:193], v[90:93]
	v_mfma_f32_16x16x32_bf16 v[78:81], v[140:143], v[198:201], v[78:81]
	v_mfma_f32_16x16x32_bf16 v[74:77], v[148:151], v[198:201], v[74:77]
	v_mfma_f32_16x16x32_bf16 v[118:121], v[152:155], v[168:171], v[118:121]
	v_mfma_f32_16x16x32_bf16 v[114:117], v[160:163], v[168:171], v[114:117]
	v_mfma_f32_16x16x32_bf16 v[102:105], v[152:155], v[176:179], v[102:105]
	v_mfma_f32_16x16x32_bf16 v[98:101], v[160:163], v[176:179], v[98:101]
	v_mfma_f32_16x16x32_bf16 v[86:89], v[152:155], v[186:189], v[86:89]
	v_mfma_f32_16x16x32_bf16 v[82:85], v[160:163], v[186:189], v[82:85]
	v_mfma_f32_16x16x32_bf16 v[70:73], v[152:155], v[194:197], v[70:73]
	v_mfma_f32_16x16x32_bf16 v[66:69], v[160:163], v[194:197], v[66:69]
	v_mfma_f32_16x16x32_bf16 v[118:121], v[156:159], v[172:175], v[118:121]
	v_mfma_f32_16x16x32_bf16 v[114:117], v[164:167], v[172:175], v[114:117]
	v_mfma_f32_16x16x32_bf16 v[102:105], v[156:159], v[182:185], v[102:105]
	v_mfma_f32_16x16x32_bf16 v[98:101], v[164:167], v[182:185], v[98:101]
	v_mfma_f32_16x16x32_bf16 v[86:89], v[156:159], v[190:193], v[86:89]
	v_mfma_f32_16x16x32_bf16 v[82:85], v[164:167], v[190:193], v[82:85]
	v_mfma_f32_16x16x32_bf16 v[70:73], v[156:159], v[198:201], v[70:73]
	v_mfma_f32_16x16x32_bf16 v[66:69], v[164:167], v[198:201], v[66:69]
	s_barrier
	s_setprio 0
	s_add_i32 s2, s2, s45
	v_lshl_add_u64 v[202:203], s[36:37], 0, v[0:1]
	s_mov_b32 m0, s2
	ds_read_b128 v[168:171], v181 offset:16384
	ds_read_b128 v[172:175], v181 offset:17408
	ds_read_b128 v[176:179], v181 offset:18432
	ds_read_b128 v[182:185], v181 offset:19456
	ds_read_b128 v[186:189], v181 offset:20480
	ds_read_b128 v[190:193], v181 offset:21504
	ds_read_b128 v[194:197], v181 offset:22528
	ds_read_b128 v[198:201], v181 offset:23552
	global_load_lds_dwordx4 v[202:203], off
	s_add_i32 m0, s2, 0x2000
	s_add_u32 s30, s36, 0x80000
	v_lshl_add_u64 v[204:205], s[36:37], 0, v[130:131]
	s_addc_u32 s31, s37, 0
	s_add_i32 s2, s67, s45
	global_load_lds_dwordx4 v[204:205], off
	v_lshl_add_u64 v[206:207], s[30:31], 0, v[0:1]
	s_mov_b32 m0, s2
	v_lshl_add_u64 v[208:209], s[38:39], 0, v[130:131]
	global_load_lds_dwordx4 v[206:207], off
	s_add_i32 m0, s2, 0x2000
	v_lshl_add_u64 v[206:207], s[30:31], 0, v[130:131]
	global_load_lds_dwordx4 v[206:207], off
	s_mov_b32 m0, s46
	v_lshl_add_u64 v[206:207], s[38:39], 0, v[0:1]
	global_load_lds_dwordx4 v[206:207], off
	s_mov_b32 m0, s47
	s_nop 0
	global_load_lds_dwordx4 v[208:209], off
	s_waitcnt vmcnt(8) lgkmcnt(0)
	s_setprio 1
	s_barrier
; #define PG8_STAGE(bufoff, gbase, voff) do { _Pragma("unroll") for (int _i = 0; _i < 2; ++_i) \
;         __builtin_amdgcn_global_load_lds((const unsigned*)((const char*)(gbase) + (voff)[_i]), (PG8_LAS unsigned*)(lds + (bufoff) + ldsw + _i * 8192), 16, 0, 0); } while (0)
; #define PG8_LDA(dst, b, h) do { _Pragma("unroll") for (int m = 0; m < 4; ++m) _Pragma("unroll") for (int k = 0; k < 2; ++k) dst[m][k] = *(const PG8_LAS bf16x8*)(lds + PG8_SA(b, h) + aoff + m * 2048 + k * 1024); } while (0)
; #define PG8_LDB(dst, b, h) do { _Pragma("unroll") for (int n = 0; n < 2; ++n) _Pragma("unroll") for (int k = 0; k < 2; ++k) dst[n][k] = *(const PG8_LAS bf16x8*)(lds + PG8_SB(b, h) + boff + n * 2048 + k * 1024); } while (0)
; #define PG8_MMA(ai, bj, At, Bt) do { __builtin_amdgcn_s_setprio(1); _Pragma("unroll") for (int m = 0; m < 4; ++m) _Pragma("unroll") for (int n = 0; n < 2; ++n) _Pragma("unroll") for (int k = 0; k < 2; ++k) \
;         acc[ai][bj][m][n] = __builtin_amdgcn_mfma_f32_16x16x32_bf16(Bt[n][k], At[m][k], acc[ai][bj][m][n], 0, 0, 0); __builtin_amdgcn_s_setprio(0); } while (0)
; #define PG8_WAIT_V(n) asm volatile("s_waitcnt vmcnt(" #n ")" ::: "memory")
; #define PG8_WAIT_L(n) asm volatile("s_waitcnt lgkmcnt(" #n ")" ::: "memory")
; #define PG8_BAR __builtin_amdgcn_s_barrier()
; #define PG8_SCHED __builtin_amdgcn_sched_barrier(0)
; template <class Epi, class Sched, bool ALIGN_EPI = false, bool SP2 = false, bool GATHER = false>
; __device__ __forceinline__ void gemm_phase(PG8_LAS unsigned char* lds, const Gemm g, const Sched& S, const Epi& E, const int2* gslot = nullptr, PG8_LAS unsigned char* gtab = nullptr) {
;     ...
;             PG8_LDA(At, 0, 1); PG8_STAGE(PG8_SB(0, 0), b2, voffB); PG8_STAGE(PG8_SB(0, 1), b2 + hstep, voffB); PG8_STAGE(PG8_SA(0, 0), a2, PG8_VA(vS, 0));
;             PG8_WAIT_V(8); PG8_WAIT_L(0); PG8_BAR; PG8_MMA(1, 0, At, B0); PG8_MMA(1, 1, At, B1); PG8_BAR; PG8_SCHED;
;             PG8_LDB(B0, 1, 0); PG8_LDB(B1, 1, 1); PG8_SCHED; PG8_LDA(At, 1, 0); PG8_STAGE(PG8_SA(0, 1), a2 + PG8_AH(1), PG8_VA(vS, 1));
;             PG8_WAIT_V(8); PG8_WAIT_L(0); PG8_BAR; PG8_MMA(0, 0, At, B0); PG8_MMA(0, 1, At, B1); PG8_BAR; PG8_SCHED;
	v_mfma_f32_16x16x32_bf16 v[62:65], v[136:139], v[168:171], v[62:65]
	v_mfma_f32_16x16x32_bf16 v[58:61], v[144:147], v[168:171], v[58:61]
	v_mfma_f32_16x16x32_bf16 v[46:49], v[136:139], v[176:179], v[46:49]
	v_mfma_f32_16x16x32_bf16 v[42:45], v[144:147], v[176:179], v[42:45]
	v_mfma_f32_16x16x32_bf16 v[30:33], v[136:139], v[186:189], v[30:33]
	v_mfma_f32_16x16x32_bf16 v[26:29], v[144:147], v[186:189], v[26:29]
	v_mfma_f32_16x16x32_bf16 v[14:17], v[136:139], v[194:197], v[14:17]
	v_mfma_f32_16x16x32_bf16 v[10:13], v[144:147], v[194:197], v[10:13]
	v_mfma_f32_16x16x32_bf16 v[62:65], v[140:143], v[172:175], v[62:65]
	v_mfma_f32_16x16x32_bf16 v[58:61], v[148:151], v[172:175], v[58:61]
	v_mfma_f32_16x16x32_bf16 v[46:49], v[140:143], v[182:185], v[46:49]
	v_mfma_f32_16x16x32_bf16 v[42:45], v[148:151], v[182:185], v[42:45]
	v_mfma_f32_16x16x32_bf16 v[30:33], v[140:143], v[190:193], v[30:33]
	v_mfma_f32_16x16x32_bf16 v[26:29], v[148:151], v[190:193], v[26:29]
	v_mfma_f32_16x16x32_bf16 v[14:17], v[140:143], v[198:201], v[14:17]
	v_mfma_f32_16x16x32_bf16 v[10:13], v[148:151], v[198:201], v[10:13]
	v_mfma_f32_16x16x32_bf16 v[54:57], v[152:155], v[168:171], v[54:57]
	v_mfma_f32_16x16x32_bf16 v[50:53], v[160:163], v[168:171], v[50:53]
	v_mfma_f32_16x16x32_bf16 v[38:41], v[152:155], v[176:179], v[38:41]
	v_mfma_f32_16x16x32_bf16 v[34:37], v[160:163], v[176:179], v[34:37]
	v_mfma_f32_16x16x32_bf16 v[22:25], v[152:155], v[186:189], v[22:25]
	v_mfma_f32_16x16x32_bf16 v[18:21], v[160:163], v[186:189], v[18:21]
	v_mfma_f32_16x16x32_bf16 v[6:9], v[152:155], v[194:197], v[6:9]
	v_mfma_f32_16x16x32_bf16 v[2:5], v[160:163], v[194:197], v[2:5]
	v_mfma_f32_16x16x32_bf16 v[54:57], v[156:159], v[172:175], v[54:57]
	v_mfma_f32_16x16x32_bf16 v[50:53], v[164:167], v[172:175], v[50:53]
	v_mfma_f32_16x16x32_bf16 v[38:41], v[156:159], v[182:185], v[38:41]
	v_mfma_f32_16x16x32_bf16 v[34:37], v[164:167], v[182:185], v[34:37]
	v_mfma_f32_16x16x32_bf16 v[22:25], v[156:159], v[190:193], v[22:25]
	v_mfma_f32_16x16x32_bf16 v[18:21], v[164:167], v[190:193], v[18:21]
	v_mfma_f32_16x16x32_bf16 v[6:9], v[156:159], v[198:201], v[6:9]
	v_mfma_f32_16x16x32_bf16 v[2:5], v[164:167], v[198:201], v[2:5]
	s_barrier
	s_setprio 0
	s_add_i32 s2, 0, 0x18000
	s_add_i32 s67, 0, 0x1c000
	v_add_u32_e32 v148, s2, v215
	v_add_u32_e32 v164, s67, v215
	ds_read_b128 v[136:139], v148
	ds_read_b128 v[140:143], v148 offset:1024
	ds_read_b128 v[144:147], v148 offset:2048
	ds_read_b128 v[148:151], v148 offset:3072
	ds_read_b128 v[152:155], v164
	ds_read_b128 v[156:159], v164 offset:1024
	ds_read_b128 v[160:163], v164 offset:2048
	ds_read_b128 v[164:167], v164 offset:3072
	s_add_u32 s30, s38, 0x80000
	s_addc_u32 s31, s39, 0
	s_mov_b32 m0, s50
	v_lshl_add_u64 v[210:211], s[30:31], 0, v[0:1]
	ds_read_b128 v[168:171], v181 offset:32768
	ds_read_b128 v[172:175], v181 offset:33792
	ds_read_b128 v[176:179], v181 offset:34816
	ds_read_b128 v[182:185], v181 offset:35840
	ds_read_b128 v[186:189], v181 offset:36864
	ds_read_b128 v[190:193], v181 offset:37888
	ds_read_b128 v[194:197], v181 offset:38912
	ds_read_b128 v[198:201], v181 offset:39936
	global_load_lds_dwordx4 v[210:211], off
	s_mov_b32 m0, s51
	v_lshl_add_u64 v[210:211], s[30:31], 0, v[130:131]
	global_load_lds_dwordx4 v[210:211], off
	s_waitcnt vmcnt(8) lgkmcnt(0)
	s_setprio 1
	s_barrier
	v_mfma_f32_16x16x32_bf16 v[126:129], v[136:139], v[168:171], v[126:129]
	v_mfma_f32_16x16x32_bf16 v[122:125], v[144:147], v[168:171], v[122:125]
	v_mfma_f32_16x16x32_bf16 v[110:113], v[136:139], v[176:179], v[110:113]
	v_mfma_f32_16x16x32_bf16 v[106:109], v[144:147], v[176:179], v[106:109]
	v_mfma_f32_16x16x32_bf16 v[94:97], v[136:139], v[186:189], v[94:97]
	v_mfma_f32_16x16x32_bf16 v[90:93], v[144:147], v[186:189], v[90:93]
	v_mfma_f32_16x16x32_bf16 v[78:81], v[136:139], v[194:197], v[78:81]
	v_mfma_f32_16x16x32_bf16 v[74:77], v[144:147], v[194:197], v[74:77]
	v_mfma_f32_16x16x32_bf16 v[126:129], v[140:143], v[172:175], v[126:129]
	v_mfma_f32_16x16x32_bf16 v[122:125], v[148:151], v[172:175], v[122:125]
	v_mfma_f32_16x16x32_bf16 v[110:113], v[140:143], v[182:185], v[110:113]
	v_mfma_f32_16x16x32_bf16 v[106:109], v[148:151], v[182:185], v[106:109]
	v_mfma_f32_16x16x32_bf16 v[94:97], v[140:143], v[190:193], v[94:97]
	v_mfma_f32_16x16x32_bf16 v[90:93], v[148:151], v[190:193], v[90:93]
	v_mfma_f32_16x16x32_bf16 v[78:81], v[140:143], v[198:201], v[78:81]
	v_mfma_f32_16x16x32_bf16 v[74:77], v[148:151], v[198:201], v[74:77]
	v_mfma_f32_16x16x32_bf16 v[118:121], v[152:155], v[168:171], v[118:121]
	v_mfma_f32_16x16x32_bf16 v[114:117], v[160:163], v[168:171], v[114:117]
	v_mfma_f32_16x16x32_bf16 v[102:105], v[152:155], v[176:179], v[102:105]
	v_mfma_f32_16x16x32_bf16 v[98:101], v[160:163], v[176:179], v[98:101]
	v_mfma_f32_16x16x32_bf16 v[86:89], v[152:155], v[186:189], v[86:89]
	v_mfma_f32_16x16x32_bf16 v[82:85], v[160:163], v[186:189], v[82:85]
	v_mfma_f32_16x16x32_bf16 v[70:73], v[152:155], v[194:197], v[70:73]
	v_mfma_f32_16x16x32_bf16 v[66:69], v[160:163], v[194:197], v[66:69]
	v_mfma_f32_16x16x32_bf16 v[118:121], v[156:159], v[172:175], v[118:121]
	v_mfma_f32_16x16x32_bf16 v[114:117], v[164:167], v[172:175], v[114:117]
	v_mfma_f32_16x16x32_bf16 v[102:105], v[156:159], v[182:185], v[102:105]
	v_mfma_f32_16x16x32_bf16 v[98:101], v[164:167], v[182:185], v[98:101]
	v_mfma_f32_16x16x32_bf16 v[86:89], v[156:159], v[190:193], v[86:89]
	v_mfma_f32_16x16x32_bf16 v[82:85], v[164:167], v[190:193], v[82:85]
	v_mfma_f32_16x16x32_bf16 v[70:73], v[156:159], v[198:201], v[70:73]
	v_mfma_f32_16x16x32_bf16 v[66:69], v[164:167], v[198:201], v[66:69]
	s_barrier
; #define PG8_STAGE(bufoff, gbase, voff) do { _Pragma("unroll") for (int _i = 0; _i < 2; ++_i) \
;         __builtin_amdgcn_global_load_lds((const unsigned*)((const char*)(gbase) + (voff)[_i]), (PG8_LAS unsigned*)(lds + (bufoff) + ldsw + _i * 8192), 16, 0, 0); } while (0)
; #define PG8_LDA(dst, b, h) do { _Pragma("unroll") for (int m = 0; m < 4; ++m) _Pragma("unroll") for (int k = 0; k < 2; ++k) dst[m][k] = *(const PG8_LAS bf16x8*)(lds + PG8_SA(b, h) + aoff + m * 2048 + k * 1024); } while (0)
; #define PG8_MMA(ai, bj, At, Bt) do { __builtin_amdgcn_s_setprio(1); _Pragma("unroll") for (int m = 0; m < 4; ++m) _Pragma("unroll") for (int n = 0; n < 2; ++n) _Pragma("unroll") for (int k = 0; k < 2; ++k) \
;         acc[ai][bj][m][n] = __builtin_amdgcn_mfma_f32_16x16x32_bf16(Bt[n][k], At[m][k], acc[ai][bj][m][n], 0, 0, 0); __builtin_amdgcn_s_setprio(0); } while (0)
; #define PG8_WAIT_V(n) asm volatile("s_waitcnt vmcnt(" #n ")" ::: "memory")
; #define PG8_WAIT_L(n) asm volatile("s_waitcnt lgkmcnt(" #n ")" ::: "memory")
; #define PG8_BAR __builtin_amdgcn_s_barrier()
; #define PG8_SCHED __builtin_amdgcn_sched_barrier(0)
; template <class Epi, class Sched, bool ALIGN_EPI = false, bool SP2 = false, bool GATHER = false>
; __device__ __forceinline__ void gemm_phase(PG8_LAS unsigned char* lds, const Gemm g, const Sched& S, const Epi& E, const int2* gslot = nullptr, PG8_LAS unsigned char* gtab = nullptr) {
;     ...
;         for (int t = 0; t < nt; t += 2) {
;             const bool last = (t == nt - 2);
;             const char* a1 = cA + (size_t)(t + 1) * kstep;
;             const char* a2 = last ? nA : cA + (size_t)(t + 2) * kstep; const char* b2 = last ? nB : cB + (size_t)(t + 2) * kstep;
;             const char* a3 = a2 + kstep; const char* b3 = b2 + kstep;
;             if (last && has_next) S.a_ready(nxt);
;     ...
;             PG8_LDA(At, 1, 1); PG8_STAGE(PG8_SB(1, 0), b3, voffB); PG8_STAGE(PG8_SB(1, 1), b3 + hstep, voffB); PG8_STAGE(PG8_SA(1, 0), a3, PG8_VA(vS, 0));
;             PG8_WAIT_V(8); PG8_WAIT_L(0); PG8_BAR; PG8_MMA(1, 0, At, B0); PG8_MMA(1, 1, At, B1); PG8_BAR; PG8_SCHED;
	s_setprio 0
	s_add_i32 s2, s2, s45
	v_lshl_add_u64 v[202:203], v[202:203], 0, s[54:55]
	s_mov_b32 m0, s2
	ds_read_b128 v[168:171], v181 offset:49152
	ds_read_b128 v[172:175], v181 offset:50176
	ds_read_b128 v[176:179], v181 offset:51200
	ds_read_b128 v[182:185], v181 offset:52224
	ds_read_b128 v[186:189], v181 offset:53248
	ds_read_b128 v[190:193], v181 offset:54272
	ds_read_b128 v[194:197], v181 offset:55296
	ds_read_b128 v[198:201], v181 offset:56320
	global_load_lds_dwordx4 v[202:203], off
	s_add_i32 m0, s2, 0x2000
	s_add_u32 s30, s36, 0x80080
	v_lshl_add_u64 v[202:203], v[204:205], 0, s[54:55]
	s_addc_u32 s31, s37, 0
	s_add_i32 s2, s67, s45
	global_load_lds_dwordx4 v[202:203], off
	s_mov_b32 m0, s2
	v_lshl_add_u64 v[202:203], s[30:31], 0, v[0:1]
	global_load_lds_dwordx4 v[202:203], off
	s_add_i32 m0, s2, 0x2000
	v_lshl_add_u64 v[202:203], s[30:31], 0, v[130:131]
	global_load_lds_dwordx4 v[202:203], off
	s_mov_b32 m0, s52
	v_lshl_add_u64 v[202:203], v[206:207], 0, s[54:55]
	global_load_lds_dwordx4 v[202:203], off
	s_mov_b32 m0, s53
	v_lshl_add_u64 v[202:203], v[208:209], 0, s[54:55]
	global_load_lds_dwordx4 v[202:203], off
	s_waitcnt vmcnt(8) lgkmcnt(0)
	s_setprio 1
	s_barrier
	v_mfma_f32_16x16x32_bf16 v[62:65], v[136:139], v[168:171], v[62:65]
	v_mfma_f32_16x16x32_bf16 v[58:61], v[144:147], v[168:171], v[58:61]
	v_mfma_f32_16x16x32_bf16 v[46:49], v[136:139], v[176:179], v[46:49]
	v_mfma_f32_16x16x32_bf16 v[42:45], v[144:147], v[176:179], v[42:45]
	v_mfma_f32_16x16x32_bf16 v[30:33], v[136:139], v[186:189], v[30:33]
	v_mfma_f32_16x16x32_bf16 v[26:29], v[144:147], v[186:189], v[26:29]
	v_mfma_f32_16x16x32_bf16 v[14:17], v[136:139], v[194:197], v[14:17]
	v_mfma_f32_16x16x32_bf16 v[10:13], v[144:147], v[194:197], v[10:13]
	v_mfma_f32_16x16x32_bf16 v[62:65], v[140:143], v[172:175], v[62:65]
	v_mfma_f32_16x16x32_bf16 v[58:61], v[148:151], v[172:175], v[58:61]
	v_mfma_f32_16x16x32_bf16 v[46:49], v[140:143], v[182:185], v[46:49]
	v_mfma_f32_16x16x32_bf16 v[42:45], v[148:151], v[182:185], v[42:45]
	v_mfma_f32_16x16x32_bf16 v[30:33], v[140:143], v[190:193], v[30:33]
	v_mfma_f32_16x16x32_bf16 v[26:29], v[148:151], v[190:193], v[26:29]
	v_mfma_f32_16x16x32_bf16 v[14:17], v[140:143], v[198:201], v[14:17]
	v_mfma_f32_16x16x32_bf16 v[10:13], v[148:151], v[198:201], v[10:13]
	v_mfma_f32_16x16x32_bf16 v[54:57], v[152:155], v[168:171], v[54:57]
	v_mfma_f32_16x16x32_bf16 v[50:53], v[160:163], v[168:171], v[50:53]
	v_mfma_f32_16x16x32_bf16 v[38:41], v[152:155], v[176:179], v[38:41]
	v_mfma_f32_16x16x32_bf16 v[34:37], v[160:163], v[176:179], v[34:37]
	v_mfma_f32_16x16x32_bf16 v[22:25], v[152:155], v[186:189], v[22:25]
	v_mfma_f32_16x16x32_bf16 v[18:21], v[160:163], v[186:189], v[18:21]
	v_mfma_f32_16x16x32_bf16 v[6:9], v[152:155], v[194:197], v[6:9]
	v_mfma_f32_16x16x32_bf16 v[2:5], v[160:163], v[194:197], v[2:5]
	v_mfma_f32_16x16x32_bf16 v[54:57], v[156:159], v[172:175], v[54:57]
	v_mfma_f32_16x16x32_bf16 v[50:53], v[164:167], v[172:175], v[50:53]
	v_mfma_f32_16x16x32_bf16 v[38:41], v[156:159], v[182:185], v[38:41]
	v_mfma_f32_16x16x32_bf16 v[34:37], v[164:167], v[182:185], v[34:37]
	v_mfma_f32_16x16x32_bf16 v[22:25], v[156:159], v[190:193], v[22:25]
	v_mfma_f32_16x16x32_bf16 v[18:21], v[164:167], v[190:193], v[18:21]
	v_mfma_f32_16x16x32_bf16 v[6:9], v[156:159], v[198:201], v[6:9]
	v_mfma_f32_16x16x32_bf16 v[2:5], v[164:167], v[198:201], v[2:5]
	s_barrier
	s_setprio 0
	s_add_i32 s66, s66, 2
	s_add_u32 s64, s64, 0x100
	s_addc_u32 s65, s65, 0
	s_cmp_gt_u32 s66, 29
	s_mov_b64 s[30:31], s[34:35]
	s_cbranch_scc0 .LBB0_482
	s_and_b64 vcc, exec, s[20:21]
	s_cbranch_vccz .LBB0_485
	s_barrier

; #define PG8_GREAD(dst, u, par) do { _Pragma("unroll") for (int h_ = 0; h_ < 2; ++h_) _Pragma("unroll") for (int i_ = 0; i_ < 2; ++i_) { const int rl_ = 128 * h_ + grl[i_]; \
;         const int tk_ = *(const PG8_LAS int*)(gtab + (par) * 2048 + rl_ * 8); const unsigned tok_ = (rl_ < (u).rows) ? ((unsigned)tk_ >> 2) : 0u; dst[h_][i_] = tok_ * (unsigned)(K * 2) + gcb[i_]; } } while (0)
; #define PG8_STAGE(bufoff, gbase, voff) do { _Pragma("unroll") for (int _i = 0; _i < 2; ++_i) \
;         __builtin_amdgcn_global_load_lds((const unsigned*)((const char*)(gbase) + (voff)[_i]), (PG8_LAS unsigned*)(lds + (bufoff) + ldsw + _i * 8192), 16, 0, 0); } while (0)
; #define PG8_WAIT_V(n) asm volatile("s_waitcnt vmcnt(" #n ")" ::: "memory")
; #define PG8_WAIT_L(n) asm volatile("s_waitcnt lgkmcnt(" #n ")" ::: "memory")
; template <class Epi, class Sched, bool ALIGN_EPI = false, bool SP2 = false, bool GATHER = false>
; __device__ __forceinline__ void gemm_phase(PG8_LAS unsigned char* lds, const Gemm g, const Sched& S, const Epi& E, const int2* gslot = nullptr, PG8_LAS unsigned char* gtab = nullptr) {
;     ...
;             const bool last = (t == nt - 2);
;             const char* a1 = cA + (size_t)(t + 1) * kstep;
;             const char* a2 = last ? nA : cA + (size_t)(t + 2) * kstep; const char* b2 = last ? nB : cB + (size_t)(t + 2) * kstep;
;             const char* a3 = a2 + kstep; const char* b3 = b2 + kstep;
;             if (last && has_next) S.a_ready(nxt);
;             if constexpr (GATHER) { if (last) { if (has_next) { PG8_GREAD(vN, nxt, (ui + 1) & 1); } else { _Pragma("unroll") for (int h_ = 0; h_ < 2; ++h_) _Pragma("unroll") for (int i_ = 0; i_ < 2; ++i_) vN[h_][i_] = vC[h_][i_]; } } }
;             unsigned vS[2][2];
; #pragma unroll
;             for (int h_ = 0; h_ < 2; ++h_)
; #pragma unroll
;                 for (int i_ = 0; i_ < 2; ++i_) vS[h_][i_] = (GATHER && last) ? vN[h_][i_] : vC[h_][i_];
;             if constexpr (SP2) {
;             PG8_LDB(B0, 0, 0); PG8_LDB(B1, 0, 1); PG8_SCHED; PG8_LDA(At, 0, 0); PG8_STAGE(PG8_SA(1, 1), a1 + PG8_AH(1), PG8_VA(vC, 1));
;             PG8_WAIT_V(8); PG8_WAIT_L(0); PG8_BAR; PG8_MMA(0, 0, At, B0); PG8_MMA(0, 1, At, B1); PG8_BAR; PG8_SCHED;
;             PG8_LDA(At, 0, 1); PG8_STAGE(PG8_SB(0, 0), b2, voffB); PG8_STAGE(PG8_SB(0, 1), b2 + hstep, voffB); PG8_STAGE(PG8_SA(0, 0), a2, PG8_VA(vS, 0));
.LBB0_565:
	s_add_u32 s2, s24, 0xfffc0080
	s_addc_u32 s26, s25, -1
	s_cmp_eq_u32 s62, 12
	s_cselect_b32 s29, s19, s26
	s_cselect_b32 s28, s53, s2
	s_cselect_b32 s27, s15, s61
	s_cselect_b32 s26, s56, s60
	s_add_i32 s2, 0, 0x10000
	v_add_u32_e32 v140, s2, v146
	s_add_i32 s63, 0, 0x14000
	ds_read_b128 v[142:145], v140
	ds_read_b128 v[150:153], v140 offset:1024
	ds_read_b128 v[154:157], v140 offset:2048
	ds_read_b128 v[158:161], v140 offset:3072
	v_add_u32_e32 v140, s63, v146
	ds_read_b128 v[162:165], v140
	ds_read_b128 v[166:169], v140 offset:1024
	ds_read_b128 v[170:173], v140 offset:2048
	ds_read_b128 v[174:177], v140 offset:3072
	v_lshl_add_u64 v[210:211], s[24:25], 0, v[136:137]
	s_add_i32 m0, s36, 0xc000
	ds_read_b128 v[178:181], v148
	ds_read_b128 v[182:185], v148 offset:1024
	ds_read_b128 v[186:189], v148 offset:2048
	ds_read_b128 v[190:193], v148 offset:3072
	ds_read_b128 v[194:197], v148 offset:4096
	ds_read_b128 v[198:201], v148 offset:5120
	ds_read_b128 v[202:205], v148 offset:6144
	ds_read_b128 v[206:209], v148 offset:7168
	global_load_lds_dwordx4 v[210:211], off
	s_add_i32 m0, s36, 0xe000
	v_lshl_add_u64 v[210:211], s[24:25], 0, v[138:139]
	global_load_lds_dwordx4 v[210:211], off
	s_waitcnt vmcnt(8) lgkmcnt(0)
	s_setprio 1
	s_barrier
	v_mfma_f32_16x16x32_bf16 v[126:129], v[142:145], v[178:181], v[126:129]
	v_mfma_f32_16x16x32_bf16 v[122:125], v[154:157], v[178:181], v[122:125]
	v_mfma_f32_16x16x32_bf16 v[114:117], v[142:145], v[186:189], v[114:117]
	v_mfma_f32_16x16x32_bf16 v[106:109], v[154:157], v[186:189], v[106:109]
	v_mfma_f32_16x16x32_bf16 v[98:101], v[142:145], v[194:197], v[98:101]
	v_mfma_f32_16x16x32_bf16 v[90:93], v[154:157], v[194:197], v[90:93]
	v_mfma_f32_16x16x32_bf16 v[82:85], v[142:145], v[202:205], v[82:85]
	v_mfma_f32_16x16x32_bf16 v[74:77], v[154:157], v[202:205], v[74:77]
	v_mfma_f32_16x16x32_bf16 v[126:129], v[150:153], v[182:185], v[126:129]
	v_mfma_f32_16x16x32_bf16 v[122:125], v[158:161], v[182:185], v[122:125]
	v_mfma_f32_16x16x32_bf16 v[114:117], v[150:153], v[190:193], v[114:117]
	v_mfma_f32_16x16x32_bf16 v[106:109], v[158:161], v[190:193], v[106:109]
	v_mfma_f32_16x16x32_bf16 v[98:101], v[150:153], v[198:201], v[98:101]
	v_mfma_f32_16x16x32_bf16 v[90:93], v[158:161], v[198:201], v[90:93]
	v_mfma_f32_16x16x32_bf16 v[82:85], v[150:153], v[206:209], v[82:85]
	v_mfma_f32_16x16x32_bf16 v[74:77], v[158:161], v[206:209], v[74:77]
	v_mfma_f32_16x16x32_bf16 v[118:121], v[162:165], v[178:181], v[118:121]
	v_mfma_f32_16x16x32_bf16 v[110:113], v[170:173], v[178:181], v[110:113]
	v_mfma_f32_16x16x32_bf16 v[102:105], v[162:165], v[186:189], v[102:105]
	v_mfma_f32_16x16x32_bf16 v[94:97], v[170:173], v[186:189], v[94:97]
	v_mfma_f32_16x16x32_bf16 v[86:89], v[162:165], v[194:197], v[86:89]
	v_mfma_f32_16x16x32_bf16 v[78:81], v[170:173], v[194:197], v[78:81]
	v_mfma_f32_16x16x32_bf16 v[70:73], v[162:165], v[202:205], v[70:73]
	v_mfma_f32_16x16x32_bf16 v[66:69], v[170:173], v[202:205], v[66:69]
	v_mfma_f32_16x16x32_bf16 v[118:121], v[166:169], v[182:185], v[118:121]
	v_mfma_f32_16x16x32_bf16 v[110:113], v[174:177], v[182:185], v[110:113]
	v_mfma_f32_16x16x32_bf16 v[102:105], v[166:169], v[190:193], v[102:105]
	v_mfma_f32_16x16x32_bf16 v[94:97], v[174:177], v[190:193], v[94:97]
	v_mfma_f32_16x16x32_bf16 v[86:89], v[166:169], v[198:201], v[86:89]
	v_mfma_f32_16x16x32_bf16 v[78:81], v[174:177], v[198:201], v[78:81]
	v_mfma_f32_16x16x32_bf16 v[70:73], v[166:169], v[206:209], v[70:73]
	v_mfma_f32_16x16x32_bf16 v[66:69], v[174:177], v[206:209], v[66:69]
	s_barrier
	s_setprio 0
	s_add_i32 s2, s2, s35
	v_lshl_add_u64 v[210:211], s[26:27], 0, v[0:1]
	s_mov_b32 m0, s2
	ds_read_b128 v[178:181], v148 offset:16384
	ds_read_b128 v[182:185], v148 offset:17408
	ds_read_b128 v[186:189], v148 offset:18432
	ds_read_b128 v[190:193], v148 offset:19456
	ds_read_b128 v[194:197], v148 offset:20480
	ds_read_b128 v[198:201], v148 offset:21504
	ds_read_b128 v[202:205], v148 offset:22528
	ds_read_b128 v[206:209], v148 offset:23552
	global_load_lds_dwordx4 v[210:211], off
	s_add_i32 m0, s2, 0x2000
	s_add_u32 s64, s26, 0x40000
	v_lshl_add_u64 v[212:213], s[26:27], 0, v[130:131]
	s_addc_u32 s65, s27, 0
	s_add_i32 s2, s63, s35
	global_load_lds_dwordx4 v[212:213], off
	v_lshl_add_u64 v[214:215], s[64:65], 0, v[0:1]
	s_mov_b32 m0, s2
	v_lshl_add_u64 v[216:217], s[28:29], 0, v[132:133]
	global_load_lds_dwordx4 v[214:215], off
	s_add_i32 m0, s2, 0x2000
	v_lshl_add_u64 v[214:215], s[64:65], 0, v[130:131]
	global_load_lds_dwordx4 v[214:215], off
	s_mov_b32 m0, s36
	v_lshl_add_u64 v[214:215], s[28:29], 0, v[134:135]
	global_load_lds_dwordx4 v[214:215], off
	s_mov_b32 m0, s37
	s_nop 0
	global_load_lds_dwordx4 v[216:217], off
	s_waitcnt vmcnt(8) lgkmcnt(0)
	s_setprio 1
	s_barrier
; #define PG8_STAGE(bufoff, gbase, voff) do { _Pragma("unroll") for (int _i = 0; _i < 2; ++_i) \
;         __builtin_amdgcn_global_load_lds((const unsigned*)((const char*)(gbase) + (voff)[_i]), (PG8_LAS unsigned*)(lds + (bufoff) + ldsw + _i * 8192), 16, 0, 0); } while (0)
; #define PG8_LDA(dst, b, h) do { _Pragma("unroll") for (int m = 0; m < 4; ++m) _Pragma("unroll") for (int k = 0; k < 2; ++k) dst[m][k] = *(const PG8_LAS bf16x8*)(lds + PG8_SA(b, h) + aoff + m * 2048 + k * 1024); } while (0)
; #define PG8_LDB(dst, b, h) do { _Pragma("unroll") for (int n = 0; n < 2; ++n) _Pragma("unroll") for (int k = 0; k < 2; ++k) dst[n][k] = *(const PG8_LAS bf16x8*)(lds + PG8_SB(b, h) + boff + n * 2048 + k * 1024); } while (0)
; #define PG8_MMA(ai, bj, At, Bt) do { __builtin_amdgcn_s_setprio(1); _Pragma("unroll") for (int m = 0; m < 4; ++m) _Pragma("unroll") for (int n = 0; n < 2; ++n) _Pragma("unroll") for (int k = 0; k < 2; ++k) \
;         acc[ai][bj][m][n] = __builtin_amdgcn_mfma_f32_16x16x32_bf16(Bt[n][k], At[m][k], acc[ai][bj][m][n], 0, 0, 0); __builtin_amdgcn_s_setprio(0); } while (0)
; #define PG8_WAIT_V(n) asm volatile("s_waitcnt vmcnt(" #n ")" ::: "memory")
; #define PG8_WAIT_L(n) asm volatile("s_waitcnt lgkmcnt(" #n ")" ::: "memory")
; #define PG8_BAR __builtin_amdgcn_s_barrier()
; #define PG8_SCHED __builtin_amdgcn_sched_barrier(0)
; template <class Epi, class Sched, bool ALIGN_EPI = false, bool SP2 = false, bool GATHER = false>
; __device__ __forceinline__ void gemm_phase(PG8_LAS unsigned char* lds, const Gemm g, const Sched& S, const Epi& E, const int2* gslot = nullptr, PG8_LAS unsigned char* gtab = nullptr) {
;     ...
;             PG8_LDA(At, 0, 1); PG8_STAGE(PG8_SB(0, 0), b2, voffB); PG8_STAGE(PG8_SB(0, 1), b2 + hstep, voffB); PG8_STAGE(PG8_SA(0, 0), a2, PG8_VA(vS, 0));
;             PG8_WAIT_V(8); PG8_WAIT_L(0); PG8_BAR; PG8_MMA(1, 0, At, B0); PG8_MMA(1, 1, At, B1); PG8_BAR; PG8_SCHED;
;             PG8_LDB(B0, 1, 0); PG8_LDB(B1, 1, 1); PG8_SCHED; PG8_LDA(At, 1, 0); PG8_STAGE(PG8_SA(0, 1), a2 + PG8_AH(1), PG8_VA(vS, 1));
;             PG8_WAIT_V(8); PG8_WAIT_L(0); PG8_BAR; PG8_MMA(0, 0, At, B0); PG8_MMA(0, 1, At, B1); PG8_BAR; PG8_SCHED;
	v_mfma_f32_16x16x32_bf16 v[62:65], v[142:145], v[178:181], v[62:65]
	v_mfma_f32_16x16x32_bf16 v[58:61], v[154:157], v[178:181], v[58:61]
	v_mfma_f32_16x16x32_bf16 v[50:53], v[142:145], v[186:189], v[50:53]
	v_mfma_f32_16x16x32_bf16 v[42:45], v[154:157], v[186:189], v[42:45]
	v_mfma_f32_16x16x32_bf16 v[34:37], v[142:145], v[194:197], v[34:37]
	v_mfma_f32_16x16x32_bf16 v[26:29], v[154:157], v[194:197], v[26:29]
	v_mfma_f32_16x16x32_bf16 v[18:21], v[142:145], v[202:205], v[18:21]
	v_mfma_f32_16x16x32_bf16 v[10:13], v[154:157], v[202:205], v[10:13]
	v_mfma_f32_16x16x32_bf16 v[62:65], v[150:153], v[182:185], v[62:65]
	v_mfma_f32_16x16x32_bf16 v[58:61], v[158:161], v[182:185], v[58:61]
	v_mfma_f32_16x16x32_bf16 v[50:53], v[150:153], v[190:193], v[50:53]
	v_mfma_f32_16x16x32_bf16 v[42:45], v[158:161], v[190:193], v[42:45]
	v_mfma_f32_16x16x32_bf16 v[34:37], v[150:153], v[198:201], v[34:37]
	v_mfma_f32_16x16x32_bf16 v[26:29], v[158:161], v[198:201], v[26:29]
	v_mfma_f32_16x16x32_bf16 v[18:21], v[150:153], v[206:209], v[18:21]
	v_mfma_f32_16x16x32_bf16 v[10:13], v[158:161], v[206:209], v[10:13]
	v_mfma_f32_16x16x32_bf16 v[54:57], v[162:165], v[178:181], v[54:57]
	v_mfma_f32_16x16x32_bf16 v[46:49], v[170:173], v[178:181], v[46:49]
	v_mfma_f32_16x16x32_bf16 v[38:41], v[162:165], v[186:189], v[38:41]
	v_mfma_f32_16x16x32_bf16 v[30:33], v[170:173], v[186:189], v[30:33]
	v_mfma_f32_16x16x32_bf16 v[22:25], v[162:165], v[194:197], v[22:25]
	v_mfma_f32_16x16x32_bf16 v[14:17], v[170:173], v[194:197], v[14:17]
	v_mfma_f32_16x16x32_bf16 v[6:9], v[162:165], v[202:205], v[6:9]
	v_mfma_f32_16x16x32_bf16 v[2:5], v[170:173], v[202:205], v[2:5]
	v_mfma_f32_16x16x32_bf16 v[54:57], v[166:169], v[182:185], v[54:57]
	v_mfma_f32_16x16x32_bf16 v[46:49], v[174:177], v[182:185], v[46:49]
	v_mfma_f32_16x16x32_bf16 v[38:41], v[166:169], v[190:193], v[38:41]
	v_mfma_f32_16x16x32_bf16 v[30:33], v[174:177], v[190:193], v[30:33]
	v_mfma_f32_16x16x32_bf16 v[22:25], v[166:169], v[198:201], v[22:25]
	v_mfma_f32_16x16x32_bf16 v[14:17], v[174:177], v[198:201], v[14:17]
	v_mfma_f32_16x16x32_bf16 v[6:9], v[166:169], v[206:209], v[6:9]
	v_mfma_f32_16x16x32_bf16 v[2:5], v[174:177], v[206:209], v[2:5]
	s_barrier
	s_setprio 0
	s_add_i32 s2, 0, 0x18000
	v_add_u32_e32 v140, s2, v146
	s_add_i32 s63, 0, 0x1c000
	ds_read_b128 v[142:145], v140
	ds_read_b128 v[150:153], v140 offset:1024
	ds_read_b128 v[154:157], v140 offset:2048
	ds_read_b128 v[158:161], v140 offset:3072
	v_add_u32_e32 v140, s63, v146
	ds_read_b128 v[162:165], v140
	ds_read_b128 v[166:169], v140 offset:1024
	ds_read_b128 v[170:173], v140 offset:2048
	ds_read_b128 v[174:177], v140 offset:3072
	s_add_u32 s28, s28, 0x40000
	s_addc_u32 s29, s29, 0
	s_mov_b32 m0, s38
	v_lshl_add_u64 v[218:219], s[28:29], 0, v[134:135]
	ds_read_b128 v[178:181], v148 offset:32768
	ds_read_b128 v[182:185], v148 offset:33792
	ds_read_b128 v[186:189], v148 offset:34816
	ds_read_b128 v[190:193], v148 offset:35840
	ds_read_b128 v[194:197], v148 offset:36864
	ds_read_b128 v[198:201], v148 offset:37888
	ds_read_b128 v[202:205], v148 offset:38912
	ds_read_b128 v[206:209], v148 offset:39936
	global_load_lds_dwordx4 v[218:219], off
	s_mov_b32 m0, s39
	v_lshl_add_u64 v[218:219], s[28:29], 0, v[132:133]
	global_load_lds_dwordx4 v[218:219], off
	s_waitcnt vmcnt(8) lgkmcnt(0)
	s_setprio 1
	s_barrier
	v_mfma_f32_16x16x32_bf16 v[126:129], v[142:145], v[178:181], v[126:129]
	v_mfma_f32_16x16x32_bf16 v[122:125], v[154:157], v[178:181], v[122:125]
	v_mfma_f32_16x16x32_bf16 v[114:117], v[142:145], v[186:189], v[114:117]
	v_mfma_f32_16x16x32_bf16 v[106:109], v[154:157], v[186:189], v[106:109]
	v_mfma_f32_16x16x32_bf16 v[98:101], v[142:145], v[194:197], v[98:101]
	v_mfma_f32_16x16x32_bf16 v[90:93], v[154:157], v[194:197], v[90:93]
	v_mfma_f32_16x16x32_bf16 v[82:85], v[142:145], v[202:205], v[82:85]
	v_mfma_f32_16x16x32_bf16 v[74:77], v[154:157], v[202:205], v[74:77]
	v_mfma_f32_16x16x32_bf16 v[126:129], v[150:153], v[182:185], v[126:129]
	v_mfma_f32_16x16x32_bf16 v[122:125], v[158:161], v[182:185], v[122:125]
	v_mfma_f32_16x16x32_bf16 v[114:117], v[150:153], v[190:193], v[114:117]
	v_mfma_f32_16x16x32_bf16 v[106:109], v[158:161], v[190:193], v[106:109]
	v_mfma_f32_16x16x32_bf16 v[98:101], v[150:153], v[198:201], v[98:101]
	v_mfma_f32_16x16x32_bf16 v[90:93], v[158:161], v[198:201], v[90:93]
	v_mfma_f32_16x16x32_bf16 v[82:85], v[150:153], v[206:209], v[82:85]
	v_mfma_f32_16x16x32_bf16 v[74:77], v[158:161], v[206:209], v[74:77]
	v_mfma_f32_16x16x32_bf16 v[118:121], v[162:165], v[178:181], v[118:121]
	v_mfma_f32_16x16x32_bf16 v[110:113], v[170:173], v[178:181], v[110:113]
	v_mfma_f32_16x16x32_bf16 v[102:105], v[162:165], v[186:189], v[102:105]
	v_mfma_f32_16x16x32_bf16 v[94:97], v[170:173], v[186:189], v[94:97]
	v_mfma_f32_16x16x32_bf16 v[86:89], v[162:165], v[194:197], v[86:89]
	v_mfma_f32_16x16x32_bf16 v[78:81], v[170:173], v[194:197], v[78:81]
	v_mfma_f32_16x16x32_bf16 v[70:73], v[162:165], v[202:205], v[70:73]
	v_mfma_f32_16x16x32_bf16 v[66:69], v[170:173], v[202:205], v[66:69]
	v_mfma_f32_16x16x32_bf16 v[118:121], v[166:169], v[182:185], v[118:121]
	v_mfma_f32_16x16x32_bf16 v[110:113], v[174:177], v[182:185], v[110:113]
	v_mfma_f32_16x16x32_bf16 v[102:105], v[166:169], v[190:193], v[102:105]
	v_mfma_f32_16x16x32_bf16 v[94:97], v[174:177], v[190:193], v[94:97]
	v_mfma_f32_16x16x32_bf16 v[86:89], v[166:169], v[198:201], v[86:89]
	v_mfma_f32_16x16x32_bf16 v[78:81], v[174:177], v[198:201], v[78:81]
	v_mfma_f32_16x16x32_bf16 v[70:73], v[166:169], v[206:209], v[70:73]
	v_mfma_f32_16x16x32_bf16 v[66:69], v[174:177], v[206:209], v[66:69]
	s_barrier
; #define PG8_STAGE(bufoff, gbase, voff) do { _Pragma("unroll") for (int _i = 0; _i < 2; ++_i) \
;         __builtin_amdgcn_global_load_lds((const unsigned*)((const char*)(gbase) + (voff)[_i]), (PG8_LAS unsigned*)(lds + (bufoff) + ldsw + _i * 8192), 16, 0, 0); } while (0)
; #define PG8_LDA(dst, b, h) do { _Pragma("unroll") for (int m = 0; m < 4; ++m) _Pragma("unroll") for (int k = 0; k < 2; ++k) dst[m][k] = *(const PG8_LAS bf16x8*)(lds + PG8_SA(b, h) + aoff + m * 2048 + k * 1024); } while (0)
; #define PG8_MMA(ai, bj, At, Bt) do { __builtin_amdgcn_s_setprio(1); _Pragma("unroll") for (int m = 0; m < 4; ++m) _Pragma("unroll") for (int n = 0; n < 2; ++n) _Pragma("unroll") for (int k = 0; k < 2; ++k) \
;         acc[ai][bj][m][n] = __builtin_amdgcn_mfma_f32_16x16x32_bf16(Bt[n][k], At[m][k], acc[ai][bj][m][n], 0, 0, 0); __builtin_amdgcn_s_setprio(0); } while (0)
; #define PG8_WAIT_V(n) asm volatile("s_waitcnt vmcnt(" #n ")" ::: "memory")
; #define PG8_WAIT_L(n) asm volatile("s_waitcnt lgkmcnt(" #n ")" ::: "memory")
; #define PG8_BAR __builtin_amdgcn_s_barrier()
; #define PG8_SCHED __builtin_amdgcn_sched_barrier(0)
; template <class Epi, class Sched, bool ALIGN_EPI = false, bool SP2 = false, bool GATHER = false>
; __device__ __forceinline__ void gemm_phase(PG8_LAS unsigned char* lds, const Gemm g, const Sched& S, const Epi& E, const int2* gslot = nullptr, PG8_LAS unsigned char* gtab = nullptr) {
;     ...
;         for (int t = 0; t < nt; t += 2) {
;             const bool last = (t == nt - 2);
;             const char* a1 = cA + (size_t)(t + 1) * kstep;
;             const char* a2 = last ? nA : cA + (size_t)(t + 2) * kstep; const char* b2 = last ? nB : cB + (size_t)(t + 2) * kstep;
;             const char* a3 = a2 + kstep; const char* b3 = b2 + kstep;
;             if (last && has_next) S.a_ready(nxt);
;     ...
;             PG8_LDA(At, 1, 1); PG8_STAGE(PG8_SB(1, 0), b3, voffB); PG8_STAGE(PG8_SB(1, 1), b3 + hstep, voffB); PG8_STAGE(PG8_SA(1, 0), a3, PG8_VA(vS, 0));
;             PG8_WAIT_V(8); PG8_WAIT_L(0); PG8_BAR; PG8_MMA(1, 0, At, B0); PG8_MMA(1, 1, At, B1); PG8_BAR; PG8_SCHED;
	s_setprio 0
	s_add_i32 s2, s2, s35
	v_lshl_add_u64 v[210:211], v[210:211], 0, s[54:55]
	s_mov_b32 m0, s2
	ds_read_b128 v[178:181], v148 offset:49152
	ds_read_b128 v[182:185], v148 offset:50176
	ds_read_b128 v[186:189], v148 offset:51200
	ds_read_b128 v[190:193], v148 offset:52224
	ds_read_b128 v[194:197], v148 offset:53248
	ds_read_b128 v[198:201], v148 offset:54272
	ds_read_b128 v[202:205], v148 offset:55296
	ds_read_b128 v[206:209], v148 offset:56320
	global_load_lds_dwordx4 v[210:211], off
	s_add_i32 m0, s2, 0x2000
	s_add_u32 s26, s26, 0x40080
	v_lshl_add_u64 v[210:211], v[212:213], 0, s[54:55]
	s_addc_u32 s27, s27, 0
	s_add_i32 s2, s63, s35
	global_load_lds_dwordx4 v[210:211], off
	s_mov_b32 m0, s2
	v_lshl_add_u64 v[210:211], s[26:27], 0, v[0:1]
	global_load_lds_dwordx4 v[210:211], off
	s_add_i32 m0, s2, 0x2000
	v_lshl_add_u64 v[210:211], s[26:27], 0, v[130:131]
	global_load_lds_dwordx4 v[210:211], off
	s_mov_b32 m0, s44
	v_lshl_add_u64 v[210:211], v[214:215], 0, s[54:55]
	global_load_lds_dwordx4 v[210:211], off
	s_mov_b32 m0, s45
	v_lshl_add_u64 v[210:211], v[216:217], 0, s[54:55]
	global_load_lds_dwordx4 v[210:211], off
	s_waitcnt vmcnt(8) lgkmcnt(0)
	s_setprio 1
	s_barrier
	v_mfma_f32_16x16x32_bf16 v[62:65], v[142:145], v[178:181], v[62:65]
	v_mfma_f32_16x16x32_bf16 v[58:61], v[154:157], v[178:181], v[58:61]
	v_mfma_f32_16x16x32_bf16 v[50:53], v[142:145], v[186:189], v[50:53]
	v_mfma_f32_16x16x32_bf16 v[42:45], v[154:157], v[186:189], v[42:45]
	v_mfma_f32_16x16x32_bf16 v[34:37], v[142:145], v[194:197], v[34:37]
	v_mfma_f32_16x16x32_bf16 v[26:29], v[154:157], v[194:197], v[26:29]
	v_mfma_f32_16x16x32_bf16 v[18:21], v[142:145], v[202:205], v[18:21]
	v_mfma_f32_16x16x32_bf16 v[10:13], v[154:157], v[202:205], v[10:13]
	v_mfma_f32_16x16x32_bf16 v[62:65], v[150:153], v[182:185], v[62:65]
	v_mfma_f32_16x16x32_bf16 v[58:61], v[158:161], v[182:185], v[58:61]
	v_mfma_f32_16x16x32_bf16 v[50:53], v[150:153], v[190:193], v[50:53]
	v_mfma_f32_16x16x32_bf16 v[42:45], v[158:161], v[190:193], v[42:45]
	v_mfma_f32_16x16x32_bf16 v[34:37], v[150:153], v[198:201], v[34:37]
	v_mfma_f32_16x16x32_bf16 v[26:29], v[158:161], v[198:201], v[26:29]
	v_mfma_f32_16x16x32_bf16 v[18:21], v[150:153], v[206:209], v[18:21]
	v_mfma_f32_16x16x32_bf16 v[10:13], v[158:161], v[206:209], v[10:13]
	v_mfma_f32_16x16x32_bf16 v[54:57], v[162:165], v[178:181], v[54:57]
	v_mfma_f32_16x16x32_bf16 v[46:49], v[170:173], v[178:181], v[46:49]
	v_mfma_f32_16x16x32_bf16 v[38:41], v[162:165], v[186:189], v[38:41]
	v_mfma_f32_16x16x32_bf16 v[30:33], v[170:173], v[186:189], v[30:33]
	v_mfma_f32_16x16x32_bf16 v[22:25], v[162:165], v[194:197], v[22:25]
	v_mfma_f32_16x16x32_bf16 v[14:17], v[170:173], v[194:197], v[14:17]
	v_mfma_f32_16x16x32_bf16 v[6:9], v[162:165], v[202:205], v[6:9]
	v_mfma_f32_16x16x32_bf16 v[2:5], v[170:173], v[202:205], v[2:5]
	v_mfma_f32_16x16x32_bf16 v[54:57], v[166:169], v[182:185], v[54:57]
	v_mfma_f32_16x16x32_bf16 v[46:49], v[174:177], v[182:185], v[46:49]
	v_mfma_f32_16x16x32_bf16 v[38:41], v[166:169], v[190:193], v[38:41]
	v_mfma_f32_16x16x32_bf16 v[30:33], v[174:177], v[190:193], v[30:33]
	v_mfma_f32_16x16x32_bf16 v[22:25], v[166:169], v[198:201], v[22:25]
	v_mfma_f32_16x16x32_bf16 v[14:17], v[174:177], v[198:201], v[14:17]
	v_mfma_f32_16x16x32_bf16 v[6:9], v[166:169], v[206:209], v[6:9]
	v_mfma_f32_16x16x32_bf16 v[2:5], v[174:177], v[206:209], v[2:5]
	s_barrier
	s_setprio 0
	s_add_i32 s62, s62, 2
	s_add_u32 s24, s24, 0x100
	s_addc_u32 s25, s25, 0
	s_add_u32 s60, s60, 0x100
	s_addc_u32 s61, s61, 0
	s_cmp_gt_u32 s62, 13
	s_cbranch_scc0 .LBB0_565
	s_and_b64 vcc, exec, s[12:13]
	s_cbranch_vccz .LBB0_568
	s_barrier

; #define PG8_GREAD(dst, u, par) do { _Pragma("unroll") for (int h_ = 0; h_ < 2; ++h_) _Pragma("unroll") for (int i_ = 0; i_ < 2; ++i_) { const int rl_ = 128 * h_ + grl[i_]; \
;         const int tk_ = *(const PG8_LAS int*)(gtab + (par) * 2048 + rl_ * 8); const unsigned tok_ = (rl_ < (u).rows) ? ((unsigned)tk_ >> 2) : 0u; dst[h_][i_] = tok_ * (unsigned)(K * 2) + gcb[i_]; } } while (0)
; #define PG8_STAGE(bufoff, gbase, voff) do { _Pragma("unroll") for (int _i = 0; _i < 2; ++_i) \
;         __builtin_amdgcn_global_load_lds((const unsigned*)((const char*)(gbase) + (voff)[_i]), (PG8_LAS unsigned*)(lds + (bufoff) + ldsw + _i * 8192), 16, 0, 0); } while (0)
; #define PG8_WAIT_V(n) asm volatile("s_waitcnt vmcnt(" #n ")" ::: "memory")
; #define PG8_WAIT_L(n) asm volatile("s_waitcnt lgkmcnt(" #n ")" ::: "memory")
; template <class Epi, class Sched, bool ALIGN_EPI = false, bool SP2 = false, bool GATHER = false>
; __device__ __forceinline__ void gemm_phase(PG8_LAS unsigned char* lds, const Gemm g, const Sched& S, const Epi& E, const int2* gslot = nullptr, PG8_LAS unsigned char* gtab = nullptr) {
;     ...
;             const bool last = (t == nt - 2);
;             const char* a1 = cA + (size_t)(t + 1) * kstep;
;             const char* a2 = last ? nA : cA + (size_t)(t + 2) * kstep; const char* b2 = last ? nB : cB + (size_t)(t + 2) * kstep;
;             const char* a3 = a2 + kstep; const char* b3 = b2 + kstep;
;             if (last && has_next) S.a_ready(nxt);
;             if constexpr (GATHER) { if (last) { if (has_next) { PG8_GREAD(vN, nxt, (ui + 1) & 1); } else { _Pragma("unroll") for (int h_ = 0; h_ < 2; ++h_) _Pragma("unroll") for (int i_ = 0; i_ < 2; ++i_) vN[h_][i_] = vC[h_][i_]; } } }
;             unsigned vS[2][2];
; #pragma unroll
;             for (int h_ = 0; h_ < 2; ++h_)
; #pragma unroll
;                 for (int i_ = 0; i_ < 2; ++i_) vS[h_][i_] = (GATHER && last) ? vN[h_][i_] : vC[h_][i_];
;             if constexpr (SP2) {
;             PG8_LDB(B0, 0, 0); PG8_LDB(B1, 0, 1); PG8_SCHED; PG8_LDA(At, 0, 0); PG8_STAGE(PG8_SA(1, 1), a1 + PG8_AH(1), PG8_VA(vC, 1));
;             PG8_WAIT_V(8); PG8_WAIT_L(0); PG8_BAR; PG8_MMA(0, 0, At, B0); PG8_MMA(0, 1, At, B1); PG8_BAR; PG8_SCHED;
;             PG8_LDA(At, 0, 1); PG8_STAGE(PG8_SB(0, 0), b2, voffB); PG8_STAGE(PG8_SB(0, 1), b2 + hstep, voffB); PG8_STAGE(PG8_SA(0, 0), a2, PG8_VA(vS, 0));
.LBB0_813:
	s_add_u32 s30, s28, 0x100
	s_addc_u32 s31, s29, 0
	s_cmp_eq_u32 s63, 12
	s_cselect_b32 s37, s23, s31
	s_cselect_b32 s36, s59, s30
	s_cselect_b32 s35, s21, s62
	s_cselect_b32 s34, s60, s61
	s_add_i32 s2, 0, 0x10000
	s_add_i32 s64, 0, 0x14000
	v_add_u32_e32 v148, s2, v215
	v_add_u32_e32 v164, s64, v215
	ds_read_b128 v[136:139], v148
	ds_read_b128 v[140:143], v148 offset:1024
	ds_read_b128 v[144:147], v148 offset:2048
	ds_read_b128 v[148:151], v148 offset:3072
	ds_read_b128 v[152:155], v164
	ds_read_b128 v[156:159], v164 offset:1024
	ds_read_b128 v[160:163], v164 offset:2048
	ds_read_b128 v[164:167], v164 offset:3072
	v_lshl_add_u64 v[202:203], s[28:29], 0, v[132:133]
	s_add_i32 m0, s44, 0xc000
	ds_read_b128 v[168:171], v181
	ds_read_b128 v[172:175], v181 offset:1024
	ds_read_b128 v[176:179], v181 offset:2048
	ds_read_b128 v[182:185], v181 offset:3072
	ds_read_b128 v[186:189], v181 offset:4096
	ds_read_b128 v[190:193], v181 offset:5120
	ds_read_b128 v[194:197], v181 offset:6144
	ds_read_b128 v[198:201], v181 offset:7168
	global_load_lds_dwordx4 v[202:203], off
	s_add_i32 m0, s44, 0xe000
	v_lshl_add_u64 v[202:203], s[28:29], 0, v[134:135]
	global_load_lds_dwordx4 v[202:203], off
	s_waitcnt vmcnt(8) lgkmcnt(0)
	s_setprio 1
	s_barrier
	v_mfma_f32_16x16x32_bf16 v[126:129], v[136:139], v[168:171], v[126:129]
	v_mfma_f32_16x16x32_bf16 v[122:125], v[144:147], v[168:171], v[122:125]
	v_mfma_f32_16x16x32_bf16 v[110:113], v[136:139], v[176:179], v[110:113]
	v_mfma_f32_16x16x32_bf16 v[106:109], v[144:147], v[176:179], v[106:109]
	v_mfma_f32_16x16x32_bf16 v[94:97], v[136:139], v[186:189], v[94:97]
	v_mfma_f32_16x16x32_bf16 v[90:93], v[144:147], v[186:189], v[90:93]
	v_mfma_f32_16x16x32_bf16 v[78:81], v[136:139], v[194:197], v[78:81]
	v_mfma_f32_16x16x32_bf16 v[74:77], v[144:147], v[194:197], v[74:77]
	v_mfma_f32_16x16x32_bf16 v[126:129], v[140:143], v[172:175], v[126:129]
	v_mfma_f32_16x16x32_bf16 v[122:125], v[148:151], v[172:175], v[122:125]
	v_mfma_f32_16x16x32_bf16 v[110:113], v[140:143], v[182:185], v[110:113]
	v_mfma_f32_16x16x32_bf16 v[106:109], v[148:151], v[182:185], v[106:109]
	v_mfma_f32_16x16x32_bf16 v[94:97], v[140:143], v[190:193], v[94:97]
	v_mfma_f32_16x16x32_bf16 v[90:93], v[148:151], v[190:193], v[90:93]
	v_mfma_f32_16x16x32_bf16 v[78:81], v[140:143], v[198:201], v[78:81]
	v_mfma_f32_16x16x32_bf16 v[74:77], v[148:151], v[198:201], v[74:77]
	v_mfma_f32_16x16x32_bf16 v[118:121], v[152:155], v[168:171], v[118:121]
	v_mfma_f32_16x16x32_bf16 v[114:117], v[160:163], v[168:171], v[114:117]
	v_mfma_f32_16x16x32_bf16 v[102:105], v[152:155], v[176:179], v[102:105]
	v_mfma_f32_16x16x32_bf16 v[98:101], v[160:163], v[176:179], v[98:101]
	v_mfma_f32_16x16x32_bf16 v[86:89], v[152:155], v[186:189], v[86:89]
	v_mfma_f32_16x16x32_bf16 v[82:85], v[160:163], v[186:189], v[82:85]
	v_mfma_f32_16x16x32_bf16 v[70:73], v[152:155], v[194:197], v[70:73]
	v_mfma_f32_16x16x32_bf16 v[66:69], v[160:163], v[194:197], v[66:69]
	v_mfma_f32_16x16x32_bf16 v[118:121], v[156:159], v[172:175], v[118:121]
	v_mfma_f32_16x16x32_bf16 v[114:117], v[164:167], v[172:175], v[114:117]
	v_mfma_f32_16x16x32_bf16 v[102:105], v[156:159], v[182:185], v[102:105]
	v_mfma_f32_16x16x32_bf16 v[98:101], v[164:167], v[182:185], v[98:101]
	v_mfma_f32_16x16x32_bf16 v[86:89], v[156:159], v[190:193], v[86:89]
	v_mfma_f32_16x16x32_bf16 v[82:85], v[164:167], v[190:193], v[82:85]
	v_mfma_f32_16x16x32_bf16 v[70:73], v[156:159], v[198:201], v[70:73]
	v_mfma_f32_16x16x32_bf16 v[66:69], v[164:167], v[198:201], v[66:69]
	s_barrier
	s_setprio 0
	s_add_i32 s2, s2, s43
	v_lshl_add_u64 v[202:203], s[34:35], 0, v[0:1]
	s_mov_b32 m0, s2
	ds_read_b128 v[168:171], v181 offset:16384
	ds_read_b128 v[172:175], v181 offset:17408
	ds_read_b128 v[176:179], v181 offset:18432
	ds_read_b128 v[182:185], v181 offset:19456
	ds_read_b128 v[186:189], v181 offset:20480
	ds_read_b128 v[190:193], v181 offset:21504
	ds_read_b128 v[194:197], v181 offset:22528
	ds_read_b128 v[198:201], v181 offset:23552
	global_load_lds_dwordx4 v[202:203], off
	s_add_i32 m0, s2, 0x2000
	s_add_u32 s28, s34, 0x40000
	v_lshl_add_u64 v[204:205], s[34:35], 0, v[130:131]
	s_addc_u32 s29, s35, 0
	s_add_i32 s2, s64, s43
	global_load_lds_dwordx4 v[204:205], off
	v_lshl_add_u64 v[206:207], s[28:29], 0, v[0:1]
	s_mov_b32 m0, s2
	v_lshl_add_u64 v[208:209], s[36:37], 0, v[130:131]
	global_load_lds_dwordx4 v[206:207], off
	s_add_i32 m0, s2, 0x2000
	v_lshl_add_u64 v[206:207], s[28:29], 0, v[130:131]
	global_load_lds_dwordx4 v[206:207], off
	s_mov_b32 m0, s44
	v_lshl_add_u64 v[206:207], s[36:37], 0, v[0:1]
	global_load_lds_dwordx4 v[206:207], off
	s_mov_b32 m0, s45
	s_nop 0
	global_load_lds_dwordx4 v[208:209], off
	s_waitcnt vmcnt(8) lgkmcnt(0)
	s_setprio 1
	s_barrier
; #define PG8_STAGE(bufoff, gbase, voff) do { _Pragma("unroll") for (int _i = 0; _i < 2; ++_i) \
;         __builtin_amdgcn_global_load_lds((const unsigned*)((const char*)(gbase) + (voff)[_i]), (PG8_LAS unsigned*)(lds + (bufoff) + ldsw + _i * 8192), 16, 0, 0); } while (0)
; #define PG8_LDA(dst, b, h) do { _Pragma("unroll") for (int m = 0; m < 4; ++m) _Pragma("unroll") for (int k = 0; k < 2; ++k) dst[m][k] = *(const PG8_LAS bf16x8*)(lds + PG8_SA(b, h) + aoff + m * 2048 + k * 1024); } while (0)
; #define PG8_LDB(dst, b, h) do { _Pragma("unroll") for (int n = 0; n < 2; ++n) _Pragma("unroll") for (int k = 0; k < 2; ++k) dst[n][k] = *(const PG8_LAS bf16x8*)(lds + PG8_SB(b, h) + boff + n * 2048 + k * 1024); } while (0)
; #define PG8_MMA(ai, bj, At, Bt) do { __builtin_amdgcn_s_setprio(1); _Pragma("unroll") for (int m = 0; m < 4; ++m) _Pragma("unroll") for (int n = 0; n < 2; ++n) _Pragma("unroll") for (int k = 0; k < 2; ++k) \
;         acc[ai][bj][m][n] = __builtin_amdgcn_mfma_f32_16x16x32_bf16(Bt[n][k], At[m][k], acc[ai][bj][m][n], 0, 0, 0); __builtin_amdgcn_s_setprio(0); } while (0)
; #define PG8_WAIT_V(n) asm volatile("s_waitcnt vmcnt(" #n ")" ::: "memory")
; #define PG8_WAIT_L(n) asm volatile("s_waitcnt lgkmcnt(" #n ")" ::: "memory")
; #define PG8_BAR __builtin_amdgcn_s_barrier()
; #define PG8_SCHED __builtin_amdgcn_sched_barrier(0)
; template <class Epi, class Sched, bool ALIGN_EPI = false, bool SP2 = false, bool GATHER = false>
; __device__ __forceinline__ void gemm_phase(PG8_LAS unsigned char* lds, const Gemm g, const Sched& S, const Epi& E, const int2* gslot = nullptr, PG8_LAS unsigned char* gtab = nullptr) {
;     ...
;             PG8_LDA(At, 0, 1); PG8_STAGE(PG8_SB(0, 0), b2, voffB); PG8_STAGE(PG8_SB(0, 1), b2 + hstep, voffB); PG8_STAGE(PG8_SA(0, 0), a2, PG8_VA(vS, 0));
;             PG8_WAIT_V(8); PG8_WAIT_L(0); PG8_BAR; PG8_MMA(1, 0, At, B0); PG8_MMA(1, 1, At, B1); PG8_BAR; PG8_SCHED;
;             PG8_LDB(B0, 1, 0); PG8_LDB(B1, 1, 1); PG8_SCHED; PG8_LDA(At, 1, 0); PG8_STAGE(PG8_SA(0, 1), a2 + PG8_AH(1), PG8_VA(vS, 1));
;             PG8_WAIT_V(8); PG8_WAIT_L(0); PG8_BAR; PG8_MMA(0, 0, At, B0); PG8_MMA(0, 1, At, B1); PG8_BAR; PG8_SCHED;
	v_mfma_f32_16x16x32_bf16 v[62:65], v[136:139], v[168:171], v[62:65]
	v_mfma_f32_16x16x32_bf16 v[58:61], v[144:147], v[168:171], v[58:61]
	v_mfma_f32_16x16x32_bf16 v[46:49], v[136:139], v[176:179], v[46:49]
	v_mfma_f32_16x16x32_bf16 v[42:45], v[144:147], v[176:179], v[42:45]
	v_mfma_f32_16x16x32_bf16 v[30:33], v[136:139], v[186:189], v[30:33]
	v_mfma_f32_16x16x32_bf16 v[26:29], v[144:147], v[186:189], v[26:29]
	v_mfma_f32_16x16x32_bf16 v[14:17], v[136:139], v[194:197], v[14:17]
	v_mfma_f32_16x16x32_bf16 v[10:13], v[144:147], v[194:197], v[10:13]
	v_mfma_f32_16x16x32_bf16 v[62:65], v[140:143], v[172:175], v[62:65]
	v_mfma_f32_16x16x32_bf16 v[58:61], v[148:151], v[172:175], v[58:61]
	v_mfma_f32_16x16x32_bf16 v[46:49], v[140:143], v[182:185], v[46:49]
	v_mfma_f32_16x16x32_bf16 v[42:45], v[148:151], v[182:185], v[42:45]
	v_mfma_f32_16x16x32_bf16 v[30:33], v[140:143], v[190:193], v[30:33]
	v_mfma_f32_16x16x32_bf16 v[26:29], v[148:151], v[190:193], v[26:29]
	v_mfma_f32_16x16x32_bf16 v[14:17], v[140:143], v[198:201], v[14:17]
	v_mfma_f32_16x16x32_bf16 v[10:13], v[148:151], v[198:201], v[10:13]
	v_mfma_f32_16x16x32_bf16 v[54:57], v[152:155], v[168:171], v[54:57]
	v_mfma_f32_16x16x32_bf16 v[50:53], v[160:163], v[168:171], v[50:53]
	v_mfma_f32_16x16x32_bf16 v[38:41], v[152:155], v[176:179], v[38:41]
	v_mfma_f32_16x16x32_bf16 v[34:37], v[160:163], v[176:179], v[34:37]
	v_mfma_f32_16x16x32_bf16 v[22:25], v[152:155], v[186:189], v[22:25]
	v_mfma_f32_16x16x32_bf16 v[18:21], v[160:163], v[186:189], v[18:21]
	v_mfma_f32_16x16x32_bf16 v[6:9], v[152:155], v[194:197], v[6:9]
	v_mfma_f32_16x16x32_bf16 v[2:5], v[160:163], v[194:197], v[2:5]
	v_mfma_f32_16x16x32_bf16 v[54:57], v[156:159], v[172:175], v[54:57]
	v_mfma_f32_16x16x32_bf16 v[50:53], v[164:167], v[172:175], v[50:53]
	v_mfma_f32_16x16x32_bf16 v[38:41], v[156:159], v[182:185], v[38:41]
	v_mfma_f32_16x16x32_bf16 v[34:37], v[164:167], v[182:185], v[34:37]
	v_mfma_f32_16x16x32_bf16 v[22:25], v[156:159], v[190:193], v[22:25]
	v_mfma_f32_16x16x32_bf16 v[18:21], v[164:167], v[190:193], v[18:21]
	v_mfma_f32_16x16x32_bf16 v[6:9], v[156:159], v[198:201], v[6:9]
	v_mfma_f32_16x16x32_bf16 v[2:5], v[164:167], v[198:201], v[2:5]
	s_barrier
	s_setprio 0
	s_add_i32 s2, 0, 0x18000
	s_add_i32 s64, 0, 0x1c000
	v_add_u32_e32 v148, s2, v215
	v_add_u32_e32 v164, s64, v215
	ds_read_b128 v[136:139], v148
	ds_read_b128 v[140:143], v148 offset:1024
	ds_read_b128 v[144:147], v148 offset:2048
	ds_read_b128 v[148:151], v148 offset:3072
	ds_read_b128 v[152:155], v164
	ds_read_b128 v[156:159], v164 offset:1024
	ds_read_b128 v[160:163], v164 offset:2048
	ds_read_b128 v[164:167], v164 offset:3072
	s_add_u32 s28, s36, 0x40000
	s_addc_u32 s29, s37, 0
	s_mov_b32 m0, s46
	v_lshl_add_u64 v[210:211], s[28:29], 0, v[0:1]
	ds_read_b128 v[168:171], v181 offset:32768
	ds_read_b128 v[172:175], v181 offset:33792
	ds_read_b128 v[176:179], v181 offset:34816
	ds_read_b128 v[182:185], v181 offset:35840
	ds_read_b128 v[186:189], v181 offset:36864
	ds_read_b128 v[190:193], v181 offset:37888
	ds_read_b128 v[194:197], v181 offset:38912
	ds_read_b128 v[198:201], v181 offset:39936
	global_load_lds_dwordx4 v[210:211], off
	s_mov_b32 m0, s47
	v_lshl_add_u64 v[210:211], s[28:29], 0, v[130:131]
	global_load_lds_dwordx4 v[210:211], off
	s_waitcnt vmcnt(8) lgkmcnt(0)
	s_setprio 1
	s_barrier
	v_mfma_f32_16x16x32_bf16 v[126:129], v[136:139], v[168:171], v[126:129]
	v_mfma_f32_16x16x32_bf16 v[122:125], v[144:147], v[168:171], v[122:125]
	v_mfma_f32_16x16x32_bf16 v[110:113], v[136:139], v[176:179], v[110:113]
	v_mfma_f32_16x16x32_bf16 v[106:109], v[144:147], v[176:179], v[106:109]
	v_mfma_f32_16x16x32_bf16 v[94:97], v[136:139], v[186:189], v[94:97]
	v_mfma_f32_16x16x32_bf16 v[90:93], v[144:147], v[186:189], v[90:93]
	v_mfma_f32_16x16x32_bf16 v[78:81], v[136:139], v[194:197], v[78:81]
	v_mfma_f32_16x16x32_bf16 v[74:77], v[144:147], v[194:197], v[74:77]
	v_mfma_f32_16x16x32_bf16 v[126:129], v[140:143], v[172:175], v[126:129]
	v_mfma_f32_16x16x32_bf16 v[122:125], v[148:151], v[172:175], v[122:125]
	v_mfma_f32_16x16x32_bf16 v[110:113], v[140:143], v[182:185], v[110:113]
	v_mfma_f32_16x16x32_bf16 v[106:109], v[148:151], v[182:185], v[106:109]
	v_mfma_f32_16x16x32_bf16 v[94:97], v[140:143], v[190:193], v[94:97]
	v_mfma_f32_16x16x32_bf16 v[90:93], v[148:151], v[190:193], v[90:93]
	v_mfma_f32_16x16x32_bf16 v[78:81], v[140:143], v[198:201], v[78:81]
	v_mfma_f32_16x16x32_bf16 v[74:77], v[148:151], v[198:201], v[74:77]
	v_mfma_f32_16x16x32_bf16 v[118:121], v[152:155], v[168:171], v[118:121]
	v_mfma_f32_16x16x32_bf16 v[114:117], v[160:163], v[168:171], v[114:117]
	v_mfma_f32_16x16x32_bf16 v[102:105], v[152:155], v[176:179], v[102:105]
	v_mfma_f32_16x16x32_bf16 v[98:101], v[160:163], v[176:179], v[98:101]
	v_mfma_f32_16x16x32_bf16 v[86:89], v[152:155], v[186:189], v[86:89]
	v_mfma_f32_16x16x32_bf16 v[82:85], v[160:163], v[186:189], v[82:85]
	v_mfma_f32_16x16x32_bf16 v[70:73], v[152:155], v[194:197], v[70:73]
	v_mfma_f32_16x16x32_bf16 v[66:69], v[160:163], v[194:197], v[66:69]
	v_mfma_f32_16x16x32_bf16 v[118:121], v[156:159], v[172:175], v[118:121]
	v_mfma_f32_16x16x32_bf16 v[114:117], v[164:167], v[172:175], v[114:117]
	v_mfma_f32_16x16x32_bf16 v[102:105], v[156:159], v[182:185], v[102:105]
	v_mfma_f32_16x16x32_bf16 v[98:101], v[164:167], v[182:185], v[98:101]
	v_mfma_f32_16x16x32_bf16 v[86:89], v[156:159], v[190:193], v[86:89]
	v_mfma_f32_16x16x32_bf16 v[82:85], v[164:167], v[190:193], v[82:85]
	v_mfma_f32_16x16x32_bf16 v[70:73], v[156:159], v[198:201], v[70:73]
	v_mfma_f32_16x16x32_bf16 v[66:69], v[164:167], v[198:201], v[66:69]
	s_barrier
; #define PG8_STAGE(bufoff, gbase, voff) do { _Pragma("unroll") for (int _i = 0; _i < 2; ++_i) \
;         __builtin_amdgcn_global_load_lds((const unsigned*)((const char*)(gbase) + (voff)[_i]), (PG8_LAS unsigned*)(lds + (bufoff) + ldsw + _i * 8192), 16, 0, 0); } while (0)
; #define PG8_LDA(dst, b, h) do { _Pragma("unroll") for (int m = 0; m < 4; ++m) _Pragma("unroll") for (int k = 0; k < 2; ++k) dst[m][k] = *(const PG8_LAS bf16x8*)(lds + PG8_SA(b, h) + aoff + m * 2048 + k * 1024); } while (0)
; #define PG8_MMA(ai, bj, At, Bt) do { __builtin_amdgcn_s_setprio(1); _Pragma("unroll") for (int m = 0; m < 4; ++m) _Pragma("unroll") for (int n = 0; n < 2; ++n) _Pragma("unroll") for (int k = 0; k < 2; ++k) \
;         acc[ai][bj][m][n] = __builtin_amdgcn_mfma_f32_16x16x32_bf16(Bt[n][k], At[m][k], acc[ai][bj][m][n], 0, 0, 0); __builtin_amdgcn_s_setprio(0); } while (0)
; #define PG8_WAIT_V(n) asm volatile("s_waitcnt vmcnt(" #n ")" ::: "memory")
; #define PG8_WAIT_L(n) asm volatile("s_waitcnt lgkmcnt(" #n ")" ::: "memory")
; #define PG8_BAR __builtin_amdgcn_s_barrier()
; #define PG8_SCHED __builtin_amdgcn_sched_barrier(0)
; template <class Epi, class Sched, bool ALIGN_EPI = false, bool SP2 = false, bool GATHER = false>
; __device__ __forceinline__ void gemm_phase(PG8_LAS unsigned char* lds, const Gemm g, const Sched& S, const Epi& E, const int2* gslot = nullptr, PG8_LAS unsigned char* gtab = nullptr) {
;     ...
;         for (int t = 0; t < nt; t += 2) {
;             const bool last = (t == nt - 2);
;             const char* a1 = cA + (size_t)(t + 1) * kstep;
;             const char* a2 = last ? nA : cA + (size_t)(t + 2) * kstep; const char* b2 = last ? nB : cB + (size_t)(t + 2) * kstep;
;             const char* a3 = a2 + kstep; const char* b3 = b2 + kstep;
;             if (last && has_next) S.a_ready(nxt);
;     ...
;             PG8_LDA(At, 1, 1); PG8_STAGE(PG8_SB(1, 0), b3, voffB); PG8_STAGE(PG8_SB(1, 1), b3 + hstep, voffB); PG8_STAGE(PG8_SA(1, 0), a3, PG8_VA(vS, 0));
;             PG8_WAIT_V(8); PG8_WAIT_L(0); PG8_BAR; PG8_MMA(1, 0, At, B0); PG8_MMA(1, 1, At, B1); PG8_BAR; PG8_SCHED;
	s_setprio 0
	s_add_i32 s2, s2, s43
	v_lshl_add_u64 v[202:203], v[202:203], 0, s[54:55]
	s_mov_b32 m0, s2
	ds_read_b128 v[168:171], v181 offset:49152
	ds_read_b128 v[172:175], v181 offset:50176
	ds_read_b128 v[176:179], v181 offset:51200
	ds_read_b128 v[182:185], v181 offset:52224
	ds_read_b128 v[186:189], v181 offset:53248
	ds_read_b128 v[190:193], v181 offset:54272
	ds_read_b128 v[194:197], v181 offset:55296
	ds_read_b128 v[198:201], v181 offset:56320
	global_load_lds_dwordx4 v[202:203], off
	s_add_i32 m0, s2, 0x2000
	s_add_u32 s28, s34, 0x40080
	v_lshl_add_u64 v[202:203], v[204:205], 0, s[54:55]
	s_addc_u32 s29, s35, 0
	s_add_i32 s2, s64, s43
	global_load_lds_dwordx4 v[202:203], off
	s_mov_b32 m0, s2
	v_lshl_add_u64 v[202:203], s[28:29], 0, v[0:1]
	global_load_lds_dwordx4 v[202:203], off
	s_add_i32 m0, s2, 0x2000
	v_lshl_add_u64 v[202:203], s[28:29], 0, v[130:131]
	global_load_lds_dwordx4 v[202:203], off
	s_mov_b32 m0, s50
	v_lshl_add_u64 v[202:203], v[206:207], 0, s[54:55]
	global_load_lds_dwordx4 v[202:203], off
	s_mov_b32 m0, s51
	v_lshl_add_u64 v[202:203], v[208:209], 0, s[54:55]
	global_load_lds_dwordx4 v[202:203], off
	s_waitcnt vmcnt(8) lgkmcnt(0)
	s_setprio 1
	s_barrier
	v_mfma_f32_16x16x32_bf16 v[62:65], v[136:139], v[168:171], v[62:65]
	v_mfma_f32_16x16x32_bf16 v[58:61], v[144:147], v[168:171], v[58:61]
	v_mfma_f32_16x16x32_bf16 v[46:49], v[136:139], v[176:179], v[46:49]
	v_mfma_f32_16x16x32_bf16 v[42:45], v[144:147], v[176:179], v[42:45]
	v_mfma_f32_16x16x32_bf16 v[30:33], v[136:139], v[186:189], v[30:33]
	v_mfma_f32_16x16x32_bf16 v[26:29], v[144:147], v[186:189], v[26:29]
	v_mfma_f32_16x16x32_bf16 v[14:17], v[136:139], v[194:197], v[14:17]
	v_mfma_f32_16x16x32_bf16 v[10:13], v[144:147], v[194:197], v[10:13]
	v_mfma_f32_16x16x32_bf16 v[62:65], v[140:143], v[172:175], v[62:65]
	v_mfma_f32_16x16x32_bf16 v[58:61], v[148:151], v[172:175], v[58:61]
	v_mfma_f32_16x16x32_bf16 v[46:49], v[140:143], v[182:185], v[46:49]
	v_mfma_f32_16x16x32_bf16 v[42:45], v[148:151], v[182:185], v[42:45]
	v_mfma_f32_16x16x32_bf16 v[30:33], v[140:143], v[190:193], v[30:33]
	v_mfma_f32_16x16x32_bf16 v[26:29], v[148:151], v[190:193], v[26:29]
	v_mfma_f32_16x16x32_bf16 v[14:17], v[140:143], v[198:201], v[14:17]
	v_mfma_f32_16x16x32_bf16 v[10:13], v[148:151], v[198:201], v[10:13]
	v_mfma_f32_16x16x32_bf16 v[54:57], v[152:155], v[168:171], v[54:57]
	v_mfma_f32_16x16x32_bf16 v[50:53], v[160:163], v[168:171], v[50:53]
	v_mfma_f32_16x16x32_bf16 v[38:41], v[152:155], v[176:179], v[38:41]
	v_mfma_f32_16x16x32_bf16 v[34:37], v[160:163], v[176:179], v[34:37]
	v_mfma_f32_16x16x32_bf16 v[22:25], v[152:155], v[186:189], v[22:25]
	v_mfma_f32_16x16x32_bf16 v[18:21], v[160:163], v[186:189], v[18:21]
	v_mfma_f32_16x16x32_bf16 v[6:9], v[152:155], v[194:197], v[6:9]
	v_mfma_f32_16x16x32_bf16 v[2:5], v[160:163], v[194:197], v[2:5]
	v_mfma_f32_16x16x32_bf16 v[54:57], v[156:159], v[172:175], v[54:57]
	v_mfma_f32_16x16x32_bf16 v[50:53], v[164:167], v[172:175], v[50:53]
	v_mfma_f32_16x16x32_bf16 v[38:41], v[156:159], v[182:185], v[38:41]
	v_mfma_f32_16x16x32_bf16 v[34:37], v[164:167], v[182:185], v[34:37]
	v_mfma_f32_16x16x32_bf16 v[22:25], v[156:159], v[190:193], v[22:25]
	v_mfma_f32_16x16x32_bf16 v[18:21], v[164:167], v[190:193], v[18:21]
	v_mfma_f32_16x16x32_bf16 v[6:9], v[156:159], v[198:201], v[6:9]
	v_mfma_f32_16x16x32_bf16 v[2:5], v[164:167], v[198:201], v[2:5]
	s_barrier
	s_setprio 0
	s_add_i32 s63, s63, 2
	s_add_u32 s61, s61, 0x100
	s_addc_u32 s62, s62, 0
	s_cmp_gt_u32 s63, 13
	s_mov_b64 s[28:29], s[30:31]
	s_cbranch_scc0 .LBB0_813
	s_and_b64 vcc, exec, s[18:19]
	s_cbranch_vccz .LBB0_816
	s_barrier

; #define PG8_GREAD(dst, u, par) do { _Pragma("unroll") for (int h_ = 0; h_ < 2; ++h_) _Pragma("unroll") for (int i_ = 0; i_ < 2; ++i_) { const int rl_ = 128 * h_ + grl[i_]; \
;         const int tk_ = *(const PG8_LAS int*)(gtab + (par) * 2048 + rl_ * 8); const unsigned tok_ = (rl_ < (u).rows) ? ((unsigned)tk_ >> 2) : 0u; dst[h_][i_] = tok_ * (unsigned)(K * 2) + gcb[i_]; } } while (0)
; #define PG8_STAGE(bufoff, gbase, voff) do { _Pragma("unroll") for (int _i = 0; _i < 2; ++_i) \
;         __builtin_amdgcn_global_load_lds((const unsigned*)((const char*)(gbase) + (voff)[_i]), (PG8_LAS unsigned*)(lds + (bufoff) + ldsw + _i * 8192), 16, 0, 0); } while (0)
; #define PG8_LDA(dst, b, h) do { _Pragma("unroll") for (int m = 0; m < 4; ++m) _Pragma("unroll") for (int k = 0; k < 2; ++k) dst[m][k] = *(const PG8_LAS bf16x8*)(lds + PG8_SA(b, h) + aoff + m * 2048 + k * 1024); } while (0)
; template <class Epi, class Sched, bool ALIGN_EPI = false, bool SP2 = false, bool GATHER = false>
; __device__ __forceinline__ void gemm_phase(PG8_LAS unsigned char* lds, const Gemm g, const Sched& S, const Epi& E, const int2* gslot = nullptr, PG8_LAS unsigned char* gtab = nullptr) {
;     ...
;             const char* a1 = cA + (size_t)(t + 1) * kstep;
;             const char* a2 = last ? nA : cA + (size_t)(t + 2) * kstep; const char* b2 = last ? nB : cB + (size_t)(t + 2) * kstep;
;             const char* a3 = a2 + kstep; const char* b3 = b2 + kstep;
;             if (last && has_next) S.a_ready(nxt);
;             if constexpr (GATHER) { if (last) { if (has_next) { PG8_GREAD(vN, nxt, (ui + 1) & 1); } else { _Pragma("unroll") for (int h_ = 0; h_ < 2; ++h_) _Pragma("unroll") for (int i_ = 0; i_ < 2; ++i_) vN[h_][i_] = vC[h_][i_]; } } }
;             unsigned vS[2][2];
; #pragma unroll
;             for (int h_ = 0; h_ < 2; ++h_)
; #pragma unroll
;                 for (int i_ = 0; i_ < 2; ++i_) vS[h_][i_] = (GATHER && last) ? vN[h_][i_] : vC[h_][i_];
;             if constexpr (SP2) {
;             PG8_LDB(B0, 0, 0); PG8_LDB(B1, 0, 1); PG8_SCHED; PG8_LDA(At, 0, 0); PG8_STAGE(PG8_SA(1, 1), a1 + PG8_AH(1), PG8_VA(vC, 1));
;             PG8_WAIT_V(8); PG8_WAIT_L(0); PG8_BAR; PG8_MMA(0, 0, At, B0); PG8_MMA(0, 1, At, B1); PG8_BAR; PG8_SCHED;
;             PG8_LDA(At, 0, 1); PG8_STAGE(PG8_SB(0, 0), b2, voffB); PG8_STAGE(PG8_SB(0, 1), b2 + hstep, voffB); PG8_STAGE(PG8_SA(0, 0), a2, PG8_VA(vS, 0));
.LBB0_1093:
	s_add_u32 s70, s18, s60
	s_addc_u32 s71, s19, s61
	s_add_u32 vcc_lo, s70, 0x34000100
	s_addc_u32 vcc_hi, s71, 0
	s_and_b64 s[70:71], s[72:73], exec
	s_cselect_b32 s71, s25, vcc_hi
	s_cselect_b32 s70, s24, vcc_lo
	s_add_u32 vcc_lo, s21, s60
	s_addc_u32 vcc_hi, s37, s61
	s_and_b64 s[72:73], s[72:73], exec
	s_cselect_b32 vcc_hi, s53, vcc_hi
	s_cselect_b32 vcc_lo, s52, vcc_lo
	s_add_i32 s72, 0, 0x10000
	v_add_u32_e32 v139, s72, v155
	s_add_i32 s2, 0, 0x14000
	ds_read_b128 v[140:143], v139
	ds_read_b128 v[162:165], v139 offset:1024
	ds_read_b128 v[180:183], v139 offset:2048
	ds_read_b128 v[188:191], v139 offset:3072
	v_add_u32_e32 v139, s2, v155
	ds_read_b128 v[192:195], v139
	ds_read_b128 v[196:199], v139 offset:1024
	ds_read_b128 v[200:203], v139 offset:2048
	ds_read_b128 v[204:207], v139 offset:3072
	v_lshl_add_u64 v[144:145], v[132:133], 0, s[60:61]
	s_add_i32 m0, s97, 0xc000
	ds_read_b128 v[208:211], v184
	ds_read_b128 v[212:215], v184 offset:1024
	ds_read_b128 v[216:219], v184 offset:2048
	ds_read_b128 v[220:223], v184 offset:3072
	ds_read_b128 v[224:227], v184 offset:4096
	ds_read_b128 v[230:233], v184 offset:5120
	ds_read_b128 v[236:239], v184 offset:6144
	ds_read_b128 v[240:243], v184 offset:7168
	global_load_lds_dwordx4 v[144:145], off
	s_add_i32 m0, s97, 0xe000
	v_lshl_add_u64 v[144:145], v[130:131], 0, s[60:61]
	global_load_lds_dwordx4 v[144:145], off
	s_waitcnt vmcnt(8) lgkmcnt(0)
	s_setprio 1
	s_barrier
	v_mfma_f32_16x16x32_bf16 v[122:125], v[140:143], v[208:211], v[122:125]
	v_mfma_f32_16x16x32_bf16 v[114:117], v[180:183], v[208:211], v[114:117]
	v_mfma_f32_16x16x32_bf16 v[106:109], v[140:143], v[216:219], v[106:109]
	v_mfma_f32_16x16x32_bf16 v[98:101], v[180:183], v[216:219], v[98:101]
	v_mfma_f32_16x16x32_bf16 v[94:97], v[140:143], v[224:227], v[94:97]
	v_mfma_f32_16x16x32_bf16 v[90:93], v[180:183], v[224:227], v[90:93]
	v_mfma_f32_16x16x32_bf16 v[86:89], v[140:143], v[236:239], v[86:89]
	v_mfma_f32_16x16x32_bf16 v[82:85], v[180:183], v[236:239], v[82:85]
	v_mfma_f32_16x16x32_bf16 v[122:125], v[162:165], v[212:215], v[122:125]
	v_mfma_f32_16x16x32_bf16 v[114:117], v[188:191], v[212:215], v[114:117]
	v_mfma_f32_16x16x32_bf16 v[106:109], v[162:165], v[220:223], v[106:109]
	v_mfma_f32_16x16x32_bf16 v[98:101], v[188:191], v[220:223], v[98:101]
	v_mfma_f32_16x16x32_bf16 v[94:97], v[162:165], v[230:233], v[94:97]
	v_mfma_f32_16x16x32_bf16 v[90:93], v[188:191], v[230:233], v[90:93]
	v_mfma_f32_16x16x32_bf16 v[86:89], v[162:165], v[240:243], v[86:89]
	v_mfma_f32_16x16x32_bf16 v[82:85], v[188:191], v[240:243], v[82:85]
	v_mfma_f32_16x16x32_bf16 v[78:81], v[192:195], v[208:211], v[78:81]
	v_mfma_f32_16x16x32_bf16 v[74:77], v[200:203], v[208:211], v[74:77]
	v_mfma_f32_16x16x32_bf16 v[70:73], v[192:195], v[216:219], v[70:73]
	v_mfma_f32_16x16x32_bf16 v[66:69], v[200:203], v[216:219], v[66:69]
	v_mfma_f32_16x16x32_bf16 v[62:65], v[192:195], v[224:227], v[62:65]
	v_mfma_f32_16x16x32_bf16 v[58:61], v[200:203], v[224:227], v[58:61]
	v_mfma_f32_16x16x32_bf16 v[54:57], v[192:195], v[236:239], v[54:57]
	v_mfma_f32_16x16x32_bf16 v[50:53], v[200:203], v[236:239], v[50:53]
	v_mfma_f32_16x16x32_bf16 v[78:81], v[196:199], v[212:215], v[78:81]
	v_mfma_f32_16x16x32_bf16 v[74:77], v[204:207], v[212:215], v[74:77]
	v_mfma_f32_16x16x32_bf16 v[70:73], v[196:199], v[220:223], v[70:73]
	v_mfma_f32_16x16x32_bf16 v[66:69], v[204:207], v[220:223], v[66:69]
	v_mfma_f32_16x16x32_bf16 v[62:65], v[196:199], v[230:233], v[62:65]
	v_mfma_f32_16x16x32_bf16 v[58:61], v[204:207], v[230:233], v[58:61]
	v_mfma_f32_16x16x32_bf16 v[54:57], v[196:199], v[240:243], v[54:57]
	v_mfma_f32_16x16x32_bf16 v[50:53], v[204:207], v[240:243], v[50:53]
	s_barrier
	s_setprio 0
	s_add_i32 s72, s72, s47
	v_lshl_add_u64 v[166:167], vcc, 0, v[148:149]
	s_mov_b32 m0, s72
	ds_read_b128 v[208:211], v184 offset:16384
	ds_read_b128 v[212:215], v184 offset:17408
	ds_read_b128 v[216:219], v184 offset:18432
	ds_read_b128 v[220:223], v184 offset:19456
	ds_read_b128 v[224:227], v184 offset:20480
	ds_read_b128 v[230:233], v184 offset:21504
	ds_read_b128 v[236:239], v184 offset:22528
	ds_read_b128 v[240:243], v184 offset:23552
	global_load_lds_dwordx4 v[166:167], off
	s_add_i32 m0, s72, 0x2000
	s_add_u32 s72, vcc_lo, 0x40000
	v_lshl_add_u64 v[244:245], vcc, 0, v[150:151]
	s_addc_u32 s73, vcc_hi, 0
	s_add_i32 s2, s2, s47
	global_load_lds_dwordx4 v[244:245], off
	v_lshl_add_u64 v[144:145], s[72:73], 0, v[148:149]
	s_mov_b32 m0, s2
	v_mov_b32_e32 v139, v1
	global_load_lds_dwordx4 v[144:145], off
	v_lshl_add_u64 v[144:145], s[72:73], 0, v[150:151]
	s_add_i32 m0, s2, 0x2000
	v_lshl_add_u64 v[246:247], s[70:71], 0, v[0:1]
	global_load_lds_dwordx4 v[144:145], off
	s_mov_b32 m0, s97
	v_lshl_add_u64 v[248:249], s[70:71], 0, v[138:139]
	global_load_lds_dwordx4 v0, s[70:71]
	s_mov_b32 m0, s66
	s_nop 0
	global_load_lds_dwordx4 v138, s[70:71]
	s_waitcnt vmcnt(8) lgkmcnt(0)
	s_setprio 1
	s_barrier
; #define PG8_STAGE(bufoff, gbase, voff) do { _Pragma("unroll") for (int _i = 0; _i < 2; ++_i) \
;         __builtin_amdgcn_global_load_lds((const unsigned*)((const char*)(gbase) + (voff)[_i]), (PG8_LAS unsigned*)(lds + (bufoff) + ldsw + _i * 8192), 16, 0, 0); } while (0)
; #define PG8_LDA(dst, b, h) do { _Pragma("unroll") for (int m = 0; m < 4; ++m) _Pragma("unroll") for (int k = 0; k < 2; ++k) dst[m][k] = *(const PG8_LAS bf16x8*)(lds + PG8_SA(b, h) + aoff + m * 2048 + k * 1024); } while (0)
; #define PG8_LDB(dst, b, h) do { _Pragma("unroll") for (int n = 0; n < 2; ++n) _Pragma("unroll") for (int k = 0; k < 2; ++k) dst[n][k] = *(const PG8_LAS bf16x8*)(lds + PG8_SB(b, h) + boff + n * 2048 + k * 1024); } while (0)
; #define PG8_MMA(ai, bj, At, Bt) do { __builtin_amdgcn_s_setprio(1); _Pragma("unroll") for (int m = 0; m < 4; ++m) _Pragma("unroll") for (int n = 0; n < 2; ++n) _Pragma("unroll") for (int k = 0; k < 2; ++k) \
;         acc[ai][bj][m][n] = __builtin_amdgcn_mfma_f32_16x16x32_bf16(Bt[n][k], At[m][k], acc[ai][bj][m][n], 0, 0, 0); __builtin_amdgcn_s_setprio(0); } while (0)
; #define PG8_WAIT_V(n) asm volatile("s_waitcnt vmcnt(" #n ")" ::: "memory")
; #define PG8_WAIT_L(n) asm volatile("s_waitcnt lgkmcnt(" #n ")" ::: "memory")
; #define PG8_BAR __builtin_amdgcn_s_barrier()
; #define PG8_SCHED __builtin_amdgcn_sched_barrier(0)
; template <class Epi, class Sched, bool ALIGN_EPI = false, bool SP2 = false, bool GATHER = false>
; __device__ __forceinline__ void gemm_phase(PG8_LAS unsigned char* lds, const Gemm g, const Sched& S, const Epi& E, const int2* gslot = nullptr, PG8_LAS unsigned char* gtab = nullptr) {
;     ...
;             PG8_LDA(At, 0, 1); PG8_STAGE(PG8_SB(0, 0), b2, voffB); PG8_STAGE(PG8_SB(0, 1), b2 + hstep, voffB); PG8_STAGE(PG8_SA(0, 0), a2, PG8_VA(vS, 0));
;             PG8_WAIT_V(8); PG8_WAIT_L(0); PG8_BAR; PG8_MMA(1, 0, At, B0); PG8_MMA(1, 1, At, B1); PG8_BAR; PG8_SCHED;
;             PG8_LDB(B0, 1, 0); PG8_LDB(B1, 1, 1); PG8_SCHED; PG8_LDA(At, 1, 0); PG8_STAGE(PG8_SA(0, 1), a2 + PG8_AH(1), PG8_VA(vS, 1));
;             PG8_WAIT_V(8); PG8_WAIT_L(0); PG8_BAR; PG8_MMA(0, 0, At, B0); PG8_MMA(0, 1, At, B1); PG8_BAR; PG8_SCHED;
	v_mfma_f32_16x16x32_bf16 v[46:49], v[140:143], v[208:211], v[46:49]
	v_mfma_f32_16x16x32_bf16 v[42:45], v[180:183], v[208:211], v[42:45]
	v_mfma_f32_16x16x32_bf16 v[38:41], v[140:143], v[216:219], v[38:41]
	v_mfma_f32_16x16x32_bf16 v[34:37], v[180:183], v[216:219], v[34:37]
	v_mfma_f32_16x16x32_bf16 v[30:33], v[140:143], v[224:227], v[30:33]
	v_mfma_f32_16x16x32_bf16 v[26:29], v[180:183], v[224:227], v[26:29]
	v_mfma_f32_16x16x32_bf16 v[6:9], v[140:143], v[236:239], v[6:9]
	v_mfma_f32_16x16x32_bf16 v[2:5], v[180:183], v[236:239], v[2:5]
	v_mfma_f32_16x16x32_bf16 v[46:49], v[162:165], v[212:215], v[46:49]
	v_mfma_f32_16x16x32_bf16 v[42:45], v[188:191], v[212:215], v[42:45]
	v_mfma_f32_16x16x32_bf16 v[38:41], v[162:165], v[220:223], v[38:41]
	v_mfma_f32_16x16x32_bf16 v[34:37], v[188:191], v[220:223], v[34:37]
	v_mfma_f32_16x16x32_bf16 v[30:33], v[162:165], v[230:233], v[30:33]
	v_mfma_f32_16x16x32_bf16 v[26:29], v[188:191], v[230:233], v[26:29]
	v_mfma_f32_16x16x32_bf16 v[6:9], v[162:165], v[240:243], v[6:9]
	v_mfma_f32_16x16x32_bf16 v[2:5], v[188:191], v[240:243], v[2:5]
	v_mfma_f32_16x16x32_bf16 v[22:25], v[192:195], v[208:211], v[22:25]
	v_mfma_f32_16x16x32_bf16 v[18:21], v[200:203], v[208:211], v[18:21]
	v_mfma_f32_16x16x32_bf16 v[14:17], v[192:195], v[216:219], v[14:17]
	v_mfma_f32_16x16x32_bf16 v[10:13], v[200:203], v[216:219], v[10:13]
	v_mfma_f32_16x16x32_bf16 v[102:105], v[192:195], v[224:227], v[102:105]
	v_mfma_f32_16x16x32_bf16 v[110:113], v[200:203], v[224:227], v[110:113]
	v_mfma_f32_16x16x32_bf16 v[118:121], v[192:195], v[236:239], v[118:121]
	v_mfma_f32_16x16x32_bf16 v[126:129], v[200:203], v[236:239], v[126:129]
	v_mfma_f32_16x16x32_bf16 v[22:25], v[196:199], v[212:215], v[22:25]
	v_mfma_f32_16x16x32_bf16 v[18:21], v[204:207], v[212:215], v[18:21]
	v_mfma_f32_16x16x32_bf16 v[14:17], v[196:199], v[220:223], v[14:17]
	v_mfma_f32_16x16x32_bf16 v[10:13], v[204:207], v[220:223], v[10:13]
	v_mfma_f32_16x16x32_bf16 v[102:105], v[196:199], v[230:233], v[102:105]
	v_mfma_f32_16x16x32_bf16 v[110:113], v[204:207], v[230:233], v[110:113]
	v_mfma_f32_16x16x32_bf16 v[118:121], v[196:199], v[240:243], v[118:121]
	v_mfma_f32_16x16x32_bf16 v[126:129], v[204:207], v[240:243], v[126:129]
	s_barrier
	s_setprio 0
	s_add_i32 s2, 0, 0x18000
	v_add_u32_e32 v0, s2, v155
	s_add_i32 s72, 0, 0x1c000
	ds_read_b128 v[138:141], v0
	ds_read_b128 v[142:145], v0 offset:1024
	ds_read_b128 v[162:165], v0 offset:2048
	ds_read_b128 v[180:183], v0 offset:3072
	v_add_u32_e32 v0, s72, v155
	ds_read_b128 v[188:191], v0
	ds_read_b128 v[192:195], v0 offset:1024
	ds_read_b128 v[196:199], v0 offset:2048
	ds_read_b128 v[200:203], v0 offset:3072
	s_mov_b32 m0, s67
	v_lshl_add_u64 v[136:137], s[70:71], 0, v[136:137]
	ds_read_b128 v[204:207], v184 offset:32768
	ds_read_b128 v[208:211], v184 offset:33792
	ds_read_b128 v[212:215], v184 offset:34816
	ds_read_b128 v[216:219], v184 offset:35840
	ds_read_b128 v[220:223], v184 offset:36864
	ds_read_b128 v[224:227], v184 offset:37888
	ds_read_b128 v[230:233], v184 offset:38912
	ds_read_b128 v[236:239], v184 offset:39936
	global_load_lds_dwordx4 v[136:137], off
	s_mov_b32 m0, s56
	v_lshl_add_u64 v[134:135], s[70:71], 0, v[134:135]
	global_load_lds_dwordx4 v[134:135], off
	s_waitcnt vmcnt(8) lgkmcnt(0)
	s_setprio 1
	s_barrier
	v_mfma_f32_16x16x32_bf16 v[122:125], v[138:141], v[204:207], v[122:125]
	v_mfma_f32_16x16x32_bf16 v[114:117], v[162:165], v[204:207], v[114:117]
	v_mfma_f32_16x16x32_bf16 v[106:109], v[138:141], v[212:215], v[106:109]
	v_mfma_f32_16x16x32_bf16 v[98:101], v[162:165], v[212:215], v[98:101]
	v_mfma_f32_16x16x32_bf16 v[94:97], v[138:141], v[220:223], v[94:97]
	v_mfma_f32_16x16x32_bf16 v[90:93], v[162:165], v[220:223], v[90:93]
	v_mfma_f32_16x16x32_bf16 v[86:89], v[138:141], v[230:233], v[86:89]
	v_mfma_f32_16x16x32_bf16 v[82:85], v[162:165], v[230:233], v[82:85]
	v_mfma_f32_16x16x32_bf16 v[122:125], v[142:145], v[208:211], v[122:125]
	v_mfma_f32_16x16x32_bf16 v[114:117], v[180:183], v[208:211], v[114:117]
	v_mfma_f32_16x16x32_bf16 v[106:109], v[142:145], v[216:219], v[106:109]
	v_mfma_f32_16x16x32_bf16 v[98:101], v[180:183], v[216:219], v[98:101]
	v_mfma_f32_16x16x32_bf16 v[94:97], v[142:145], v[224:227], v[94:97]
	v_mfma_f32_16x16x32_bf16 v[90:93], v[180:183], v[224:227], v[90:93]
	v_mfma_f32_16x16x32_bf16 v[86:89], v[142:145], v[236:239], v[86:89]
	v_mfma_f32_16x16x32_bf16 v[82:85], v[180:183], v[236:239], v[82:85]
	v_mfma_f32_16x16x32_bf16 v[78:81], v[188:191], v[204:207], v[78:81]
	v_mfma_f32_16x16x32_bf16 v[74:77], v[196:199], v[204:207], v[74:77]
	v_mfma_f32_16x16x32_bf16 v[70:73], v[188:191], v[212:215], v[70:73]
	v_mfma_f32_16x16x32_bf16 v[66:69], v[196:199], v[212:215], v[66:69]
	v_mfma_f32_16x16x32_bf16 v[62:65], v[188:191], v[220:223], v[62:65]
	v_mfma_f32_16x16x32_bf16 v[58:61], v[196:199], v[220:223], v[58:61]
	v_mfma_f32_16x16x32_bf16 v[54:57], v[188:191], v[230:233], v[54:57]
	v_mfma_f32_16x16x32_bf16 v[50:53], v[196:199], v[230:233], v[50:53]
	v_mfma_f32_16x16x32_bf16 v[78:81], v[192:195], v[208:211], v[78:81]
	v_mfma_f32_16x16x32_bf16 v[74:77], v[200:203], v[208:211], v[74:77]
	v_mfma_f32_16x16x32_bf16 v[70:73], v[192:195], v[216:219], v[70:73]
	v_mfma_f32_16x16x32_bf16 v[66:69], v[200:203], v[216:219], v[66:69]
	v_mfma_f32_16x16x32_bf16 v[62:65], v[192:195], v[224:227], v[62:65]
	v_mfma_f32_16x16x32_bf16 v[58:61], v[200:203], v[224:227], v[58:61]
	v_mfma_f32_16x16x32_bf16 v[54:57], v[192:195], v[236:239], v[54:57]
	v_mfma_f32_16x16x32_bf16 v[50:53], v[200:203], v[236:239], v[50:53]
	s_barrier
; #define PG8_STAGE(bufoff, gbase, voff) do { _Pragma("unroll") for (int _i = 0; _i < 2; ++_i) \
;         __builtin_amdgcn_global_load_lds((const unsigned*)((const char*)(gbase) + (voff)[_i]), (PG8_LAS unsigned*)(lds + (bufoff) + ldsw + _i * 8192), 16, 0, 0); } while (0)
; #define PG8_LDA(dst, b, h) do { _Pragma("unroll") for (int m = 0; m < 4; ++m) _Pragma("unroll") for (int k = 0; k < 2; ++k) dst[m][k] = *(const PG8_LAS bf16x8*)(lds + PG8_SA(b, h) + aoff + m * 2048 + k * 1024); } while (0)
; #define PG8_MMA(ai, bj, At, Bt) do { __builtin_amdgcn_s_setprio(1); _Pragma("unroll") for (int m = 0; m < 4; ++m) _Pragma("unroll") for (int n = 0; n < 2; ++n) _Pragma("unroll") for (int k = 0; k < 2; ++k) \
;         acc[ai][bj][m][n] = __builtin_amdgcn_mfma_f32_16x16x32_bf16(Bt[n][k], At[m][k], acc[ai][bj][m][n], 0, 0, 0); __builtin_amdgcn_s_setprio(0); } while (0)
; #define PG8_WAIT_V(n) asm volatile("s_waitcnt vmcnt(" #n ")" ::: "memory")
; #define PG8_WAIT_L(n) asm volatile("s_waitcnt lgkmcnt(" #n ")" ::: "memory")
; #define PG8_BAR __builtin_amdgcn_s_barrier()
; #define PG8_SCHED __builtin_amdgcn_sched_barrier(0)
; template <class Epi, class Sched, bool ALIGN_EPI = false, bool SP2 = false, bool GATHER = false>
; __device__ __forceinline__ void gemm_phase(PG8_LAS unsigned char* lds, const Gemm g, const Sched& S, const Epi& E, const int2* gslot = nullptr, PG8_LAS unsigned char* gtab = nullptr) {
;     ...
;         for (int t = 0; t < nt; t += 2) {
;             const bool last = (t == nt - 2);
;             const char* a1 = cA + (size_t)(t + 1) * kstep;
;             const char* a2 = last ? nA : cA + (size_t)(t + 2) * kstep; const char* b2 = last ? nB : cB + (size_t)(t + 2) * kstep;
;             const char* a3 = a2 + kstep; const char* b3 = b2 + kstep;
;             if (last && has_next) S.a_ready(nxt);
;     ...
;             PG8_LDA(At, 1, 1); PG8_STAGE(PG8_SB(1, 0), b3, voffB); PG8_STAGE(PG8_SB(1, 1), b3 + hstep, voffB); PG8_STAGE(PG8_SA(1, 0), a3, PG8_VA(vS, 0));
;             PG8_WAIT_V(8); PG8_WAIT_L(0); PG8_BAR; PG8_MMA(1, 0, At, B0); PG8_MMA(1, 1, At, B1); PG8_BAR; PG8_SCHED;
	s_setprio 0
	s_add_i32 s2, s2, s47
	v_lshl_add_u64 v[166:167], v[166:167], 0, s[54:55]
	s_mov_b32 m0, s2
	ds_read_b128 v[134:137], v184 offset:49152
	ds_read_b128 v[204:207], v184 offset:50176
	ds_read_b128 v[208:211], v184 offset:51200
	ds_read_b128 v[212:215], v184 offset:52224
	ds_read_b128 v[216:219], v184 offset:53248
	ds_read_b128 v[220:223], v184 offset:54272
	ds_read_b128 v[224:227], v184 offset:55296
	ds_read_b128 v[230:233], v184 offset:56320
	global_load_lds_dwordx4 v[166:167], off
	s_add_i32 m0, s2, 0x2000
	s_add_u32 s70, vcc_lo, 0x40080
	v_lshl_add_u64 v[166:167], v[244:245], 0, s[54:55]
	s_addc_u32 s71, vcc_hi, 0
	s_add_i32 s2, s72, s47
	global_load_lds_dwordx4 v[166:167], off
	s_mov_b32 m0, s2
	v_lshl_add_u64 v[166:167], s[70:71], 0, v[148:149]
	global_load_lds_dwordx4 v[166:167], off
	s_add_i32 m0, s2, 0x2000
	v_lshl_add_u64 v[166:167], s[70:71], 0, v[150:151]
	global_load_lds_dwordx4 v[166:167], off
	s_mov_b32 m0, s0
	v_lshl_add_u64 v[166:167], v[246:247], 0, s[54:55]
	global_load_lds_dwordx4 v[166:167], off
	s_mov_b32 m0, s43
	v_lshl_add_u64 v[166:167], v[248:249], 0, s[54:55]
	global_load_lds_dwordx4 v[166:167], off
	s_waitcnt vmcnt(8) lgkmcnt(0)
	s_setprio 1
	s_barrier
	v_mfma_f32_16x16x32_bf16 v[46:49], v[138:141], v[134:137], v[46:49]
	v_mfma_f32_16x16x32_bf16 v[42:45], v[162:165], v[134:137], v[42:45]
	v_mfma_f32_16x16x32_bf16 v[38:41], v[138:141], v[208:211], v[38:41]
	v_mfma_f32_16x16x32_bf16 v[34:37], v[162:165], v[208:211], v[34:37]
	v_mfma_f32_16x16x32_bf16 v[30:33], v[138:141], v[216:219], v[30:33]
	v_mfma_f32_16x16x32_bf16 v[26:29], v[162:165], v[216:219], v[26:29]
	v_mfma_f32_16x16x32_bf16 v[6:9], v[138:141], v[224:227], v[6:9]
	v_mfma_f32_16x16x32_bf16 v[2:5], v[162:165], v[224:227], v[2:5]
	v_mfma_f32_16x16x32_bf16 v[46:49], v[142:145], v[204:207], v[46:49]
	v_mfma_f32_16x16x32_bf16 v[42:45], v[180:183], v[204:207], v[42:45]
	v_mfma_f32_16x16x32_bf16 v[38:41], v[142:145], v[212:215], v[38:41]
	v_mfma_f32_16x16x32_bf16 v[34:37], v[180:183], v[212:215], v[34:37]
	v_mfma_f32_16x16x32_bf16 v[30:33], v[142:145], v[220:223], v[30:33]
	v_mfma_f32_16x16x32_bf16 v[26:29], v[180:183], v[220:223], v[26:29]
	v_mfma_f32_16x16x32_bf16 v[6:9], v[142:145], v[230:233], v[6:9]
	v_mfma_f32_16x16x32_bf16 v[2:5], v[180:183], v[230:233], v[2:5]
	v_mfma_f32_16x16x32_bf16 v[22:25], v[188:191], v[134:137], v[22:25]
	v_mfma_f32_16x16x32_bf16 v[18:21], v[196:199], v[134:137], v[18:21]
	v_mfma_f32_16x16x32_bf16 v[14:17], v[188:191], v[208:211], v[14:17]
	v_mfma_f32_16x16x32_bf16 v[10:13], v[196:199], v[208:211], v[10:13]
	v_mfma_f32_16x16x32_bf16 v[102:105], v[188:191], v[216:219], v[102:105]
	v_mfma_f32_16x16x32_bf16 v[110:113], v[196:199], v[216:219], v[110:113]
	v_mfma_f32_16x16x32_bf16 v[118:121], v[188:191], v[224:227], v[118:121]
	v_mfma_f32_16x16x32_bf16 v[126:129], v[196:199], v[224:227], v[126:129]
	v_mfma_f32_16x16x32_bf16 v[22:25], v[192:195], v[204:207], v[22:25]
	v_mfma_f32_16x16x32_bf16 v[18:21], v[200:203], v[204:207], v[18:21]
	v_mfma_f32_16x16x32_bf16 v[14:17], v[192:195], v[212:215], v[14:17]
	v_mfma_f32_16x16x32_bf16 v[10:13], v[200:203], v[212:215], v[10:13]
	v_mfma_f32_16x16x32_bf16 v[102:105], v[192:195], v[220:223], v[102:105]
	v_mfma_f32_16x16x32_bf16 v[110:113], v[200:203], v[220:223], v[110:113]
	v_mfma_f32_16x16x32_bf16 v[118:121], v[192:195], v[230:233], v[118:121]
	v_mfma_f32_16x16x32_bf16 v[126:129], v[200:203], v[230:233], v[126:129]
	s_barrier
	s_setprio 0
	s_add_i32 s69, s69, 2
	s_add_u32 s60, s60, 0x100
	s_addc_u32 s61, s61, 0
	s_cmp_gt_u32 s69, 13
	s_cbranch_scc1 .LBB0_1097

; #define PG8_GREAD(dst, u, par) do { _Pragma("unroll") for (int h_ = 0; h_ < 2; ++h_) _Pragma("unroll") for (int i_ = 0; i_ < 2; ++i_) { const int rl_ = 128 * h_ + grl[i_]; \
;         const int tk_ = *(const PG8_LAS int*)(gtab + (par) * 2048 + rl_ * 8); const unsigned tok_ = (rl_ < (u).rows) ? ((unsigned)tk_ >> 2) : 0u; dst[h_][i_] = tok_ * (unsigned)(K * 2) + gcb[i_]; } } while (0)
; #define PG8_STAGE(bufoff, gbase, voff) do { _Pragma("unroll") for (int _i = 0; _i < 2; ++_i) \
;         __builtin_amdgcn_global_load_lds((const unsigned*)((const char*)(gbase) + (voff)[_i]), (PG8_LAS unsigned*)(lds + (bufoff) + ldsw + _i * 8192), 16, 0, 0); } while (0)
; #define PG8_WAIT_V(n) asm volatile("s_waitcnt vmcnt(" #n ")" ::: "memory")
; #define PG8_WAIT_L(n) asm volatile("s_waitcnt lgkmcnt(" #n ")" ::: "memory")
; template <class Epi, class Sched, bool ALIGN_EPI = false, bool SP2 = false, bool GATHER = false>
; __device__ __forceinline__ void gemm_phase(PG8_LAS unsigned char* lds, const Gemm g, const Sched& S, const Epi& E, const int2* gslot = nullptr, PG8_LAS unsigned char* gtab = nullptr) {
;     ...
;             const bool last = (t == nt - 2);
;             const char* a1 = cA + (size_t)(t + 1) * kstep;
;             const char* a2 = last ? nA : cA + (size_t)(t + 2) * kstep; const char* b2 = last ? nB : cB + (size_t)(t + 2) * kstep;
;             const char* a3 = a2 + kstep; const char* b3 = b2 + kstep;
;             if (last && has_next) S.a_ready(nxt);
;             if constexpr (GATHER) { if (last) { if (has_next) { PG8_GREAD(vN, nxt, (ui + 1) & 1); } else { _Pragma("unroll") for (int h_ = 0; h_ < 2; ++h_) _Pragma("unroll") for (int i_ = 0; i_ < 2; ++i_) vN[h_][i_] = vC[h_][i_]; } } }
;             unsigned vS[2][2];
; #pragma unroll
;             for (int h_ = 0; h_ < 2; ++h_)
; #pragma unroll
;                 for (int i_ = 0; i_ < 2; ++i_) vS[h_][i_] = (GATHER && last) ? vN[h_][i_] : vC[h_][i_];
;             if constexpr (SP2) {
;             PG8_LDB(B0, 0, 0); PG8_LDB(B1, 0, 1); PG8_SCHED; PG8_LDA(At, 0, 0); PG8_STAGE(PG8_SA(1, 1), a1 + PG8_AH(1), PG8_VA(vC, 1));
;             PG8_WAIT_V(8); PG8_WAIT_L(0); PG8_BAR; PG8_MMA(0, 0, At, B0); PG8_MMA(0, 1, At, B1); PG8_BAR; PG8_SCHED;
;             PG8_LDA(At, 0, 1); PG8_STAGE(PG8_SB(0, 0), b2, voffB); PG8_STAGE(PG8_SB(0, 1), b2 + hstep, voffB); PG8_STAGE(PG8_SA(0, 0), a2, PG8_VA(vS, 0));
.LBB0_1174:
	s_add_u32 s2, s12, 0xfffc0080
	s_addc_u32 s10, s13, -1
	s_cmp_eq_u32 s67, 12
	s_cselect_b32 s15, s7, s10
	s_cselect_b32 s14, s9, s2
	s_cselect_b32 s11, s18, s29
	s_cselect_b32 s10, s19, s27
	s_add_i32 s2, 0, 0x10000
	s_add_i32 s70, 0, 0x14000
	v_add_u32_e32 v78, s2, v168
	v_add_u32_e32 v164, s70, v168
	ds_read_b128 v[66:69], v78
	ds_read_b128 v[70:73], v78 offset:1024
	ds_read_b128 v[74:77], v78 offset:2048
	ds_read_b128 v[78:81], v78 offset:3072
	ds_read_b128 v[156:159], v164
	ds_read_b128 v[160:163], v164 offset:1024
	ds_read_b128 v[172:175], v164 offset:2048
	ds_read_b128 v[176:179], v164 offset:3072
	v_lshl_add_u64 v[164:165], s[12:13], 0, v[152:153]
	s_add_i32 m0, s47, 0xc000
	ds_read_b128 v[180:183], v170
	ds_read_b128 v[184:187], v170 offset:1024
	ds_read_b128 v[188:191], v170 offset:2048
	ds_read_b128 v[192:195], v170 offset:3072
	ds_read_b128 v[196:199], v170 offset:4096
	ds_read_b128 v[200:203], v170 offset:5120
	ds_read_b128 v[204:207], v170 offset:6144
	ds_read_b128 v[208:211], v170 offset:7168
	global_load_lds_dwordx4 v[164:165], off
	s_add_i32 m0, s47, 0xe000
	v_lshl_add_u64 v[164:165], s[12:13], 0, v[154:155]
	global_load_lds_dwordx4 v[164:165], off
	s_waitcnt vmcnt(8) lgkmcnt(0)
	s_setprio 1
	s_barrier
	v_mfma_f32_16x16x32_bf16 v[142:145], v[66:69], v[180:183], v[142:145]
	v_mfma_f32_16x16x32_bf16 v[138:141], v[74:77], v[180:183], v[138:141]
	v_mfma_f32_16x16x32_bf16 v[126:129], v[66:69], v[188:191], v[126:129]
	v_mfma_f32_16x16x32_bf16 v[122:125], v[74:77], v[188:191], v[122:125]
	v_mfma_f32_16x16x32_bf16 v[110:113], v[66:69], v[196:199], v[110:113]
	v_mfma_f32_16x16x32_bf16 v[106:109], v[74:77], v[196:199], v[106:109]
	v_mfma_f32_16x16x32_bf16 v[94:97], v[66:69], v[204:207], v[94:97]
	v_mfma_f32_16x16x32_bf16 v[90:93], v[74:77], v[204:207], v[90:93]
	v_mfma_f32_16x16x32_bf16 v[142:145], v[70:73], v[184:187], v[142:145]
	v_mfma_f32_16x16x32_bf16 v[138:141], v[78:81], v[184:187], v[138:141]
	v_mfma_f32_16x16x32_bf16 v[126:129], v[70:73], v[192:195], v[126:129]
	v_mfma_f32_16x16x32_bf16 v[122:125], v[78:81], v[192:195], v[122:125]
	v_mfma_f32_16x16x32_bf16 v[110:113], v[70:73], v[200:203], v[110:113]
	v_mfma_f32_16x16x32_bf16 v[106:109], v[78:81], v[200:203], v[106:109]
	v_mfma_f32_16x16x32_bf16 v[94:97], v[70:73], v[208:211], v[94:97]
	v_mfma_f32_16x16x32_bf16 v[90:93], v[78:81], v[208:211], v[90:93]
	v_mfma_f32_16x16x32_bf16 v[134:137], v[156:159], v[180:183], v[134:137]
	v_mfma_f32_16x16x32_bf16 v[130:133], v[172:175], v[180:183], v[130:133]
	v_mfma_f32_16x16x32_bf16 v[118:121], v[156:159], v[188:191], v[118:121]
	v_mfma_f32_16x16x32_bf16 v[114:117], v[172:175], v[188:191], v[114:117]
	v_mfma_f32_16x16x32_bf16 v[102:105], v[156:159], v[196:199], v[102:105]
	v_mfma_f32_16x16x32_bf16 v[98:101], v[172:175], v[196:199], v[98:101]
	v_mfma_f32_16x16x32_bf16 v[86:89], v[156:159], v[204:207], v[86:89]
	v_mfma_f32_16x16x32_bf16 v[82:85], v[172:175], v[204:207], v[82:85]
	v_mfma_f32_16x16x32_bf16 v[134:137], v[160:163], v[184:187], v[134:137]
	v_mfma_f32_16x16x32_bf16 v[130:133], v[176:179], v[184:187], v[130:133]
	v_mfma_f32_16x16x32_bf16 v[118:121], v[160:163], v[192:195], v[118:121]
	v_mfma_f32_16x16x32_bf16 v[114:117], v[176:179], v[192:195], v[114:117]
	v_mfma_f32_16x16x32_bf16 v[102:105], v[160:163], v[200:203], v[102:105]
	v_mfma_f32_16x16x32_bf16 v[98:101], v[176:179], v[200:203], v[98:101]
	v_mfma_f32_16x16x32_bf16 v[86:89], v[160:163], v[208:211], v[86:89]
	v_mfma_f32_16x16x32_bf16 v[82:85], v[176:179], v[208:211], v[82:85]
	s_barrier
	s_setprio 0
	s_add_i32 s2, s2, s45
	v_lshl_add_u64 v[164:165], s[10:11], 0, v[0:1]
	s_mov_b32 m0, s2
	ds_read_b128 v[180:183], v170 offset:16384
	ds_read_b128 v[184:187], v170 offset:17408
	ds_read_b128 v[188:191], v170 offset:18432
	ds_read_b128 v[192:195], v170 offset:19456
	ds_read_b128 v[196:199], v170 offset:20480
	ds_read_b128 v[200:203], v170 offset:21504
	ds_read_b128 v[204:207], v170 offset:22528
	ds_read_b128 v[208:211], v170 offset:23552
	global_load_lds_dwordx4 v[164:165], off
	s_add_i32 m0, s2, 0x2000
	s_add_u32 s68, s10, 0x40000
	v_lshl_add_u64 v[212:213], s[10:11], 0, v[146:147]
	s_addc_u32 s69, s11, 0
	s_add_i32 s2, s70, s45
	global_load_lds_dwordx4 v[212:213], off
	v_lshl_add_u64 v[214:215], s[68:69], 0, v[0:1]
	s_mov_b32 m0, s2
	v_lshl_add_u64 v[216:217], s[14:15], 0, v[148:149]
	global_load_lds_dwordx4 v[214:215], off
	s_add_i32 m0, s2, 0x2000
	v_lshl_add_u64 v[214:215], s[68:69], 0, v[146:147]
	global_load_lds_dwordx4 v[214:215], off
	s_mov_b32 m0, s47
	v_lshl_add_u64 v[214:215], s[14:15], 0, v[150:151]
	global_load_lds_dwordx4 v[214:215], off
	s_mov_b32 m0, s50
	s_nop 0
	global_load_lds_dwordx4 v[216:217], off
	s_waitcnt vmcnt(8) lgkmcnt(0)
	s_setprio 1
	s_barrier
; #define PG8_STAGE(bufoff, gbase, voff) do { _Pragma("unroll") for (int _i = 0; _i < 2; ++_i) \
;         __builtin_amdgcn_global_load_lds((const unsigned*)((const char*)(gbase) + (voff)[_i]), (PG8_LAS unsigned*)(lds + (bufoff) + ldsw + _i * 8192), 16, 0, 0); } while (0)
; #define PG8_LDA(dst, b, h) do { _Pragma("unroll") for (int m = 0; m < 4; ++m) _Pragma("unroll") for (int k = 0; k < 2; ++k) dst[m][k] = *(const PG8_LAS bf16x8*)(lds + PG8_SA(b, h) + aoff + m * 2048 + k * 1024); } while (0)
; #define PG8_LDB(dst, b, h) do { _Pragma("unroll") for (int n = 0; n < 2; ++n) _Pragma("unroll") for (int k = 0; k < 2; ++k) dst[n][k] = *(const PG8_LAS bf16x8*)(lds + PG8_SB(b, h) + boff + n * 2048 + k * 1024); } while (0)
; #define PG8_MMA(ai, bj, At, Bt) do { __builtin_amdgcn_s_setprio(1); _Pragma("unroll") for (int m = 0; m < 4; ++m) _Pragma("unroll") for (int n = 0; n < 2; ++n) _Pragma("unroll") for (int k = 0; k < 2; ++k) \
;         acc[ai][bj][m][n] = __builtin_amdgcn_mfma_f32_16x16x32_bf16(Bt[n][k], At[m][k], acc[ai][bj][m][n], 0, 0, 0); __builtin_amdgcn_s_setprio(0); } while (0)
; #define PG8_WAIT_V(n) asm volatile("s_waitcnt vmcnt(" #n ")" ::: "memory")
; #define PG8_WAIT_L(n) asm volatile("s_waitcnt lgkmcnt(" #n ")" ::: "memory")
; #define PG8_BAR __builtin_amdgcn_s_barrier()
; #define PG8_SCHED __builtin_amdgcn_sched_barrier(0)
; template <class Epi, class Sched, bool ALIGN_EPI = false, bool SP2 = false, bool GATHER = false>
; __device__ __forceinline__ void gemm_phase(PG8_LAS unsigned char* lds, const Gemm g, const Sched& S, const Epi& E, const int2* gslot = nullptr, PG8_LAS unsigned char* gtab = nullptr) {
;     ...
;             PG8_LDA(At, 0, 1); PG8_STAGE(PG8_SB(0, 0), b2, voffB); PG8_STAGE(PG8_SB(0, 1), b2 + hstep, voffB); PG8_STAGE(PG8_SA(0, 0), a2, PG8_VA(vS, 0));
;             PG8_WAIT_V(8); PG8_WAIT_L(0); PG8_BAR; PG8_MMA(1, 0, At, B0); PG8_MMA(1, 1, At, B1); PG8_BAR; PG8_SCHED;
;             PG8_LDB(B0, 1, 0); PG8_LDB(B1, 1, 1); PG8_SCHED; PG8_LDA(At, 1, 0); PG8_STAGE(PG8_SA(0, 1), a2 + PG8_AH(1), PG8_VA(vS, 1));
;             PG8_WAIT_V(8); PG8_WAIT_L(0); PG8_BAR; PG8_MMA(0, 0, At, B0); PG8_MMA(0, 1, At, B1); PG8_BAR; PG8_SCHED;
	v_mfma_f32_16x16x32_bf16 v[62:65], v[66:69], v[180:183], v[62:65]
	v_mfma_f32_16x16x32_bf16 v[58:61], v[74:77], v[180:183], v[58:61]
	v_mfma_f32_16x16x32_bf16 v[46:49], v[66:69], v[188:191], v[46:49]
	v_mfma_f32_16x16x32_bf16 v[42:45], v[74:77], v[188:191], v[42:45]
	v_mfma_f32_16x16x32_bf16 v[30:33], v[66:69], v[196:199], v[30:33]
	v_mfma_f32_16x16x32_bf16 v[26:29], v[74:77], v[196:199], v[26:29]
	v_mfma_f32_16x16x32_bf16 v[14:17], v[66:69], v[204:207], v[14:17]
	v_mfma_f32_16x16x32_bf16 v[10:13], v[74:77], v[204:207], v[10:13]
	v_mfma_f32_16x16x32_bf16 v[62:65], v[70:73], v[184:187], v[62:65]
	v_mfma_f32_16x16x32_bf16 v[58:61], v[78:81], v[184:187], v[58:61]
	v_mfma_f32_16x16x32_bf16 v[46:49], v[70:73], v[192:195], v[46:49]
	v_mfma_f32_16x16x32_bf16 v[42:45], v[78:81], v[192:195], v[42:45]
	v_mfma_f32_16x16x32_bf16 v[30:33], v[70:73], v[200:203], v[30:33]
	v_mfma_f32_16x16x32_bf16 v[26:29], v[78:81], v[200:203], v[26:29]
	v_mfma_f32_16x16x32_bf16 v[14:17], v[70:73], v[208:211], v[14:17]
	v_mfma_f32_16x16x32_bf16 v[10:13], v[78:81], v[208:211], v[10:13]
	v_mfma_f32_16x16x32_bf16 v[54:57], v[156:159], v[180:183], v[54:57]
	v_mfma_f32_16x16x32_bf16 v[50:53], v[172:175], v[180:183], v[50:53]
	v_mfma_f32_16x16x32_bf16 v[38:41], v[156:159], v[188:191], v[38:41]
	v_mfma_f32_16x16x32_bf16 v[34:37], v[172:175], v[188:191], v[34:37]
	v_mfma_f32_16x16x32_bf16 v[22:25], v[156:159], v[196:199], v[22:25]
	v_mfma_f32_16x16x32_bf16 v[18:21], v[172:175], v[196:199], v[18:21]
	v_mfma_f32_16x16x32_bf16 v[6:9], v[156:159], v[204:207], v[6:9]
	v_mfma_f32_16x16x32_bf16 v[2:5], v[172:175], v[204:207], v[2:5]
	v_mfma_f32_16x16x32_bf16 v[54:57], v[160:163], v[184:187], v[54:57]
	v_mfma_f32_16x16x32_bf16 v[50:53], v[176:179], v[184:187], v[50:53]
	v_mfma_f32_16x16x32_bf16 v[38:41], v[160:163], v[192:195], v[38:41]
	v_mfma_f32_16x16x32_bf16 v[34:37], v[176:179], v[192:195], v[34:37]
	v_mfma_f32_16x16x32_bf16 v[22:25], v[160:163], v[200:203], v[22:25]
	v_mfma_f32_16x16x32_bf16 v[18:21], v[176:179], v[200:203], v[18:21]
	v_mfma_f32_16x16x32_bf16 v[6:9], v[160:163], v[208:211], v[6:9]
	v_mfma_f32_16x16x32_bf16 v[2:5], v[176:179], v[208:211], v[2:5]
	s_barrier
	s_setprio 0
	s_add_i32 s2, 0, 0x18000
	s_add_i32 s68, 0, 0x1c000
	v_add_u32_e32 v78, s2, v168
	v_add_u32_e32 v171, s68, v168
	ds_read_b128 v[66:69], v78
	ds_read_b128 v[70:73], v78 offset:1024
	ds_read_b128 v[74:77], v78 offset:2048
	ds_read_b128 v[78:81], v78 offset:3072
	ds_read_b128 v[156:159], v171
	ds_read_b128 v[160:163], v171 offset:1024
	ds_read_b128 v[172:175], v171 offset:2048
	ds_read_b128 v[176:179], v171 offset:3072
	s_add_u32 s14, s14, 0x40000
	s_addc_u32 s15, s15, 0
	s_mov_b32 m0, s51
	v_lshl_add_u64 v[218:219], s[14:15], 0, v[150:151]
	ds_read_b128 v[180:183], v170 offset:32768
	ds_read_b128 v[184:187], v170 offset:33792
	ds_read_b128 v[188:191], v170 offset:34816
	ds_read_b128 v[192:195], v170 offset:35840
	ds_read_b128 v[196:199], v170 offset:36864
	ds_read_b128 v[200:203], v170 offset:37888
	ds_read_b128 v[204:207], v170 offset:38912
	ds_read_b128 v[208:211], v170 offset:39936
	global_load_lds_dwordx4 v[218:219], off
	s_mov_b32 m0, s52
	v_lshl_add_u64 v[218:219], s[14:15], 0, v[148:149]
	global_load_lds_dwordx4 v[218:219], off
	s_waitcnt vmcnt(8) lgkmcnt(0)
	s_setprio 1
	s_barrier
	v_mfma_f32_16x16x32_bf16 v[142:145], v[66:69], v[180:183], v[142:145]
	v_mfma_f32_16x16x32_bf16 v[138:141], v[74:77], v[180:183], v[138:141]
	v_mfma_f32_16x16x32_bf16 v[126:129], v[66:69], v[188:191], v[126:129]
	v_mfma_f32_16x16x32_bf16 v[122:125], v[74:77], v[188:191], v[122:125]
	v_mfma_f32_16x16x32_bf16 v[110:113], v[66:69], v[196:199], v[110:113]
	v_mfma_f32_16x16x32_bf16 v[106:109], v[74:77], v[196:199], v[106:109]
	v_mfma_f32_16x16x32_bf16 v[94:97], v[66:69], v[204:207], v[94:97]
	v_mfma_f32_16x16x32_bf16 v[90:93], v[74:77], v[204:207], v[90:93]
	v_mfma_f32_16x16x32_bf16 v[142:145], v[70:73], v[184:187], v[142:145]
	v_mfma_f32_16x16x32_bf16 v[138:141], v[78:81], v[184:187], v[138:141]
	v_mfma_f32_16x16x32_bf16 v[126:129], v[70:73], v[192:195], v[126:129]
	v_mfma_f32_16x16x32_bf16 v[122:125], v[78:81], v[192:195], v[122:125]
	v_mfma_f32_16x16x32_bf16 v[110:113], v[70:73], v[200:203], v[110:113]
	v_mfma_f32_16x16x32_bf16 v[106:109], v[78:81], v[200:203], v[106:109]
	v_mfma_f32_16x16x32_bf16 v[94:97], v[70:73], v[208:211], v[94:97]
	v_mfma_f32_16x16x32_bf16 v[90:93], v[78:81], v[208:211], v[90:93]
	v_mfma_f32_16x16x32_bf16 v[134:137], v[156:159], v[180:183], v[134:137]
	v_mfma_f32_16x16x32_bf16 v[130:133], v[172:175], v[180:183], v[130:133]
	v_mfma_f32_16x16x32_bf16 v[118:121], v[156:159], v[188:191], v[118:121]
	v_mfma_f32_16x16x32_bf16 v[114:117], v[172:175], v[188:191], v[114:117]
	v_mfma_f32_16x16x32_bf16 v[102:105], v[156:159], v[196:199], v[102:105]
	v_mfma_f32_16x16x32_bf16 v[98:101], v[172:175], v[196:199], v[98:101]
	v_mfma_f32_16x16x32_bf16 v[86:89], v[156:159], v[204:207], v[86:89]
	v_mfma_f32_16x16x32_bf16 v[82:85], v[172:175], v[204:207], v[82:85]
	v_mfma_f32_16x16x32_bf16 v[134:137], v[160:163], v[184:187], v[134:137]
	v_mfma_f32_16x16x32_bf16 v[130:133], v[176:179], v[184:187], v[130:133]
	v_mfma_f32_16x16x32_bf16 v[118:121], v[160:163], v[192:195], v[118:121]
	v_mfma_f32_16x16x32_bf16 v[114:117], v[176:179], v[192:195], v[114:117]
	v_mfma_f32_16x16x32_bf16 v[102:105], v[160:163], v[200:203], v[102:105]
	v_mfma_f32_16x16x32_bf16 v[98:101], v[176:179], v[200:203], v[98:101]
	v_mfma_f32_16x16x32_bf16 v[86:89], v[160:163], v[208:211], v[86:89]
	v_mfma_f32_16x16x32_bf16 v[82:85], v[176:179], v[208:211], v[82:85]
	s_barrier
; #define PG8_STAGE(bufoff, gbase, voff) do { _Pragma("unroll") for (int _i = 0; _i < 2; ++_i) \
;         __builtin_amdgcn_global_load_lds((const unsigned*)((const char*)(gbase) + (voff)[_i]), (PG8_LAS unsigned*)(lds + (bufoff) + ldsw + _i * 8192), 16, 0, 0); } while (0)
; #define PG8_LDA(dst, b, h) do { _Pragma("unroll") for (int m = 0; m < 4; ++m) _Pragma("unroll") for (int k = 0; k < 2; ++k) dst[m][k] = *(const PG8_LAS bf16x8*)(lds + PG8_SA(b, h) + aoff + m * 2048 + k * 1024); } while (0)
; #define PG8_MMA(ai, bj, At, Bt) do { __builtin_amdgcn_s_setprio(1); _Pragma("unroll") for (int m = 0; m < 4; ++m) _Pragma("unroll") for (int n = 0; n < 2; ++n) _Pragma("unroll") for (int k = 0; k < 2; ++k) \
;         acc[ai][bj][m][n] = __builtin_amdgcn_mfma_f32_16x16x32_bf16(Bt[n][k], At[m][k], acc[ai][bj][m][n], 0, 0, 0); __builtin_amdgcn_s_setprio(0); } while (0)
; #define PG8_WAIT_V(n) asm volatile("s_waitcnt vmcnt(" #n ")" ::: "memory")
; #define PG8_WAIT_L(n) asm volatile("s_waitcnt lgkmcnt(" #n ")" ::: "memory")
; #define PG8_BAR __builtin_amdgcn_s_barrier()
; #define PG8_SCHED __builtin_amdgcn_sched_barrier(0)
; template <class Epi, class Sched, bool ALIGN_EPI = false, bool SP2 = false, bool GATHER = false>
; __device__ __forceinline__ void gemm_phase(PG8_LAS unsigned char* lds, const Gemm g, const Sched& S, const Epi& E, const int2* gslot = nullptr, PG8_LAS unsigned char* gtab = nullptr) {
;     ...
;         for (int t = 0; t < nt; t += 2) {
;             const bool last = (t == nt - 2);
;             const char* a1 = cA + (size_t)(t + 1) * kstep;
;             const char* a2 = last ? nA : cA + (size_t)(t + 2) * kstep; const char* b2 = last ? nB : cB + (size_t)(t + 2) * kstep;
;             const char* a3 = a2 + kstep; const char* b3 = b2 + kstep;
;             if (last && has_next) S.a_ready(nxt);
;     ...
;             PG8_LDA(At, 1, 1); PG8_STAGE(PG8_SB(1, 0), b3, voffB); PG8_STAGE(PG8_SB(1, 1), b3 + hstep, voffB); PG8_STAGE(PG8_SA(1, 0), a3, PG8_VA(vS, 0));
;             PG8_WAIT_V(8); PG8_WAIT_L(0); PG8_BAR; PG8_MMA(1, 0, At, B0); PG8_MMA(1, 1, At, B1); PG8_BAR; PG8_SCHED;
	s_setprio 0
	s_add_i32 s2, s2, s45
	v_lshl_add_u64 v[164:165], v[164:165], 0, s[54:55]
	s_mov_b32 m0, s2
	ds_read_b128 v[180:183], v170 offset:49152
	ds_read_b128 v[184:187], v170 offset:50176
	ds_read_b128 v[188:191], v170 offset:51200
	ds_read_b128 v[192:195], v170 offset:52224
	ds_read_b128 v[196:199], v170 offset:53248
	ds_read_b128 v[200:203], v170 offset:54272
	ds_read_b128 v[204:207], v170 offset:55296
	ds_read_b128 v[208:211], v170 offset:56320
	global_load_lds_dwordx4 v[164:165], off
	s_add_i32 m0, s2, 0x2000
	s_add_u32 s10, s10, 0x40080
	v_lshl_add_u64 v[164:165], v[212:213], 0, s[54:55]
	s_addc_u32 s11, s11, 0
	s_add_i32 s2, s68, s45
	global_load_lds_dwordx4 v[164:165], off
	s_mov_b32 m0, s2
	v_lshl_add_u64 v[164:165], s[10:11], 0, v[0:1]
	global_load_lds_dwordx4 v[164:165], off
	s_add_i32 m0, s2, 0x2000
	v_lshl_add_u64 v[164:165], s[10:11], 0, v[146:147]
	global_load_lds_dwordx4 v[164:165], off
	s_mov_b32 m0, s58
	v_lshl_add_u64 v[164:165], v[214:215], 0, s[54:55]
	global_load_lds_dwordx4 v[164:165], off
	s_mov_b32 m0, s59
	v_lshl_add_u64 v[164:165], v[216:217], 0, s[54:55]
	global_load_lds_dwordx4 v[164:165], off
	s_waitcnt vmcnt(8) lgkmcnt(0)
	s_setprio 1
	s_barrier
	v_mfma_f32_16x16x32_bf16 v[62:65], v[66:69], v[180:183], v[62:65]
	v_mfma_f32_16x16x32_bf16 v[58:61], v[74:77], v[180:183], v[58:61]
	v_mfma_f32_16x16x32_bf16 v[46:49], v[66:69], v[188:191], v[46:49]
	v_mfma_f32_16x16x32_bf16 v[42:45], v[74:77], v[188:191], v[42:45]
	v_mfma_f32_16x16x32_bf16 v[30:33], v[66:69], v[196:199], v[30:33]
	v_mfma_f32_16x16x32_bf16 v[26:29], v[74:77], v[196:199], v[26:29]
	v_mfma_f32_16x16x32_bf16 v[14:17], v[66:69], v[204:207], v[14:17]
	v_mfma_f32_16x16x32_bf16 v[10:13], v[74:77], v[204:207], v[10:13]
	v_mfma_f32_16x16x32_bf16 v[62:65], v[70:73], v[184:187], v[62:65]
	v_mfma_f32_16x16x32_bf16 v[58:61], v[78:81], v[184:187], v[58:61]
	v_mfma_f32_16x16x32_bf16 v[46:49], v[70:73], v[192:195], v[46:49]
	v_mfma_f32_16x16x32_bf16 v[42:45], v[78:81], v[192:195], v[42:45]
	v_mfma_f32_16x16x32_bf16 v[30:33], v[70:73], v[200:203], v[30:33]
	v_mfma_f32_16x16x32_bf16 v[26:29], v[78:81], v[200:203], v[26:29]
	v_mfma_f32_16x16x32_bf16 v[14:17], v[70:73], v[208:211], v[14:17]
	v_mfma_f32_16x16x32_bf16 v[10:13], v[78:81], v[208:211], v[10:13]
	v_mfma_f32_16x16x32_bf16 v[54:57], v[156:159], v[180:183], v[54:57]
	v_mfma_f32_16x16x32_bf16 v[50:53], v[172:175], v[180:183], v[50:53]
	v_mfma_f32_16x16x32_bf16 v[38:41], v[156:159], v[188:191], v[38:41]
	v_mfma_f32_16x16x32_bf16 v[34:37], v[172:175], v[188:191], v[34:37]
	v_mfma_f32_16x16x32_bf16 v[22:25], v[156:159], v[196:199], v[22:25]
	v_mfma_f32_16x16x32_bf16 v[18:21], v[172:175], v[196:199], v[18:21]
	v_mfma_f32_16x16x32_bf16 v[6:9], v[156:159], v[204:207], v[6:9]
	v_mfma_f32_16x16x32_bf16 v[2:5], v[172:175], v[204:207], v[2:5]
	v_mfma_f32_16x16x32_bf16 v[54:57], v[160:163], v[184:187], v[54:57]
	v_mfma_f32_16x16x32_bf16 v[50:53], v[176:179], v[184:187], v[50:53]
	v_mfma_f32_16x16x32_bf16 v[38:41], v[160:163], v[192:195], v[38:41]
	v_mfma_f32_16x16x32_bf16 v[34:37], v[176:179], v[192:195], v[34:37]
	v_mfma_f32_16x16x32_bf16 v[22:25], v[160:163], v[200:203], v[22:25]
	v_mfma_f32_16x16x32_bf16 v[18:21], v[176:179], v[200:203], v[18:21]
	v_mfma_f32_16x16x32_bf16 v[6:9], v[160:163], v[208:211], v[6:9]
	v_mfma_f32_16x16x32_bf16 v[2:5], v[176:179], v[208:211], v[2:5]
	s_barrier
	s_setprio 0
	s_add_i32 s67, s67, 2
	s_add_u32 s12, s12, 0x100
	s_addc_u32 s13, s13, 0
	s_add_u32 s27, s27, 0x100
	s_addc_u32 s29, s29, 0
	s_cmp_gt_u32 s67, 13
	s_cbranch_scc0 .LBB0_1174
	s_and_b64 vcc, exec, s[24:25]
	s_cbranch_vccz .LBB0_1177
	s_barrier
